# stack: attention claim one unit ahead; MOE1 gather loads batched; first K-iteration peeled with C=0 (no acc zeroing) in 5 GEMM phases; MOE2 and FINAL reuse MOE1 expert tables in LDS; PROJ stagger
# baseline (speedup 1.0000x reference)
.LBB0_282:
	v_mov_b32_e32 v211, v199
	v_mov_b32_e32 v213, v199
	s_mov_b32 s3, -2
	s_mov_b64 s[14:15], 0x1cc00080
	ds_read_b128 v[18:21], v223
	s_waitcnt lgkmcnt(0)
	ds_read_b128 v[22:25], v223 offset:1024
	ds_read_b128 v[26:29], v223 offset:2048
	ds_read_b128 v[30:33], v223 offset:3072
	ds_read_b128 v[2:5], v224
	ds_read_b128 v[6:9], v224 offset:1024
	ds_read_b128 v[10:13], v224 offset:2048
	ds_read_b128 v[14:17], v224 offset:3072
	s_add_i32 m0, s73, 0xc000
	s_add_u32 s16, s22, s14
	s_addc_u32 s17, s23, s15
	ds_read_b128 v[58:61], v225
	ds_read_b128 v[62:65], v225 offset:1024
	ds_read_b128 v[50:53], v225 offset:2048
	ds_read_b128 v[54:57], v225 offset:3072
	ds_read_b128 v[42:45], v225 offset:4096
	ds_read_b128 v[46:49], v225 offset:5120
	ds_read_b128 v[34:37], v225 offset:6144
	ds_read_b128 v[38:41], v225 offset:7168
	global_load_lds_dwordx4 v202, s[16:17]
	s_add_i32 m0, s73, 0xe000
	s_cmp_eq_u32 s3, 12
	global_load_lds_dwordx4 v204, s[16:17]
	s_cselect_b64 s[16:17], -1, 0
	s_cmp_lg_u32 s3, 12
	v_mov_b32_e32 v203, v199
	v_mov_b32_e32 v205, v199
	v_mov_b64_e32 v[214:215], v[204:205]
	v_mov_b64_e32 v[216:217], v[202:203]
	s_waitcnt vmcnt(8)
	s_waitcnt lgkmcnt(0)
	s_add_i32 s18, s14, 0xe3400080
	s_and_b64 s[16:17], s[16:17], exec
	s_cselect_b32 s28, 0, s18
	s_barrier
	s_setprio 1
	s_waitcnt lgkmcnt(0)
	v_mfma_f32_16x16x128_f8f6f4 v[190:193], v[18:25], v[58:65], 0
	v_mfma_f32_16x16x128_f8f6f4 v[186:189], v[26:33], v[58:65], 0
	v_mfma_f32_16x16x128_f8f6f4 v[174:177], v[18:25], v[50:57], 0
	v_mfma_f32_16x16x128_f8f6f4 v[170:173], v[26:33], v[50:57], 0
	v_mfma_f32_16x16x128_f8f6f4 v[158:161], v[18:25], v[42:49], 0
	v_mfma_f32_16x16x128_f8f6f4 v[154:157], v[26:33], v[42:49], 0
	v_mfma_f32_16x16x128_f8f6f4 v[142:145], v[18:25], v[34:41], 0
	v_mfma_f32_16x16x128_f8f6f4 v[138:141], v[26:33], v[34:41], 0
	s_setprio 0
	s_setprio 1
	v_mfma_f32_16x16x128_f8f6f4 v[182:185], v[2:9], v[58:65], 0
	v_mfma_f32_16x16x128_f8f6f4 v[178:181], v[10:17], v[58:65], 0
	v_mfma_f32_16x16x128_f8f6f4 v[166:169], v[2:9], v[50:57], 0
	v_mfma_f32_16x16x128_f8f6f4 v[162:165], v[10:17], v[50:57], 0
	v_mfma_f32_16x16x128_f8f6f4 v[150:153], v[2:9], v[42:49], 0
	v_mfma_f32_16x16x128_f8f6f4 v[146:149], v[10:17], v[42:49], 0
	v_mfma_f32_16x16x128_f8f6f4 v[134:137], v[2:9], v[34:41], 0
	v_mfma_f32_16x16x128_f8f6f4 v[130:133], v[10:17], v[34:41], 0
	s_setprio 0
	s_barrier
	s_add_u32 s16, s26, s28
	s_addc_u32 s17, s27, 0
	s_mov_b32 m0, s82
	v_lshl_add_u64 v[234:235], s[16:17], 0, v[194:195]
	s_add_u32 s18, s16, 0x40000
	ds_read_b128 v[34:37], v225 offset:16384
	ds_read_b128 v[38:41], v225 offset:17408
	ds_read_b128 v[42:45], v225 offset:18432
	ds_read_b128 v[46:49], v225 offset:19456
	ds_read_b128 v[50:53], v225 offset:20480
	ds_read_b128 v[54:57], v225 offset:21504
	ds_read_b128 v[58:61], v225 offset:22528
	ds_read_b128 v[62:65], v225 offset:23552
	global_load_lds_dwordx4 v[234:235], off
	v_lshl_add_u64 v[236:237], s[16:17], 0, v[196:197]
	s_mov_b32 m0, s83
	s_addc_u32 s19, s17, 0
	global_load_lds_dwordx4 v[236:237], off
	v_lshl_add_u64 v[238:239], s[18:19], 0, v[194:195]
	s_mov_b32 m0, s84
	v_mov_b32_e32 v201, v199
	global_load_lds_dwordx4 v[238:239], off
	v_lshl_add_u64 v[238:239], s[18:19], 0, v[196:197]
	s_mov_b32 m0, s85
	s_add_u32 s18, s24, s28
	global_load_lds_dwordx4 v[238:239], off
	s_addc_u32 s19, s25, 0
	s_mov_b32 m0, s73
	s_nop 0
	global_load_lds_dwordx4 v198, s[18:19]
	s_mov_b32 m0, s86
	s_nop 0
	global_load_lds_dwordx4 v200, s[18:19]
	s_waitcnt vmcnt(8)
	s_waitcnt lgkmcnt(0)
	s_barrier
	s_setprio 1
	s_waitcnt lgkmcnt(0)
	v_mfma_f32_16x16x128_f8f6f4 v[126:129], v[18:25], v[34:41], 0
	v_mfma_f32_16x16x128_f8f6f4 v[122:125], v[26:33], v[34:41], 0
	v_mfma_f32_16x16x128_f8f6f4 v[110:113], v[18:25], v[42:49], 0
	v_mfma_f32_16x16x128_f8f6f4 v[106:109], v[26:33], v[42:49], 0
	v_mfma_f32_16x16x128_f8f6f4 v[94:97], v[18:25], v[50:57], 0
	v_mfma_f32_16x16x128_f8f6f4 v[90:93], v[26:33], v[50:57], 0
	v_mfma_f32_16x16x128_f8f6f4 v[78:81], v[18:25], v[58:65], 0
	v_mfma_f32_16x16x128_f8f6f4 v[74:77], v[26:33], v[58:65], 0
	s_setprio 0
	s_setprio 1
	v_mfma_f32_16x16x128_f8f6f4 v[118:121], v[2:9], v[34:41], 0
	v_mfma_f32_16x16x128_f8f6f4 v[114:117], v[10:17], v[34:41], 0
	v_mfma_f32_16x16x128_f8f6f4 v[102:105], v[2:9], v[42:49], 0
	v_mfma_f32_16x16x128_f8f6f4 v[98:101], v[10:17], v[42:49], 0
	v_mfma_f32_16x16x128_f8f6f4 v[86:89], v[2:9], v[50:57], 0
	v_mfma_f32_16x16x128_f8f6f4 v[82:85], v[10:17], v[50:57], 0
	v_mfma_f32_16x16x128_f8f6f4 v[70:73], v[2:9], v[58:65], 0
	v_mfma_f32_16x16x128_f8f6f4 v[66:69], v[10:17], v[58:65], 0
	s_setprio 0
	s_barrier
	s_add_i32 s33, 0, 0x18000
	s_add_i32 s40, 0, 0x1c000
	v_add_u32_e32 v14, s33, v220
	v_add_u32_e32 v30, s40, v220
	ds_read_b128 v[2:5], v14
	ds_read_b128 v[6:9], v14 offset:1024
	ds_read_b128 v[10:13], v14 offset:2048
	ds_read_b128 v[14:17], v14 offset:3072
	ds_read_b128 v[18:21], v30
	ds_read_b128 v[22:25], v30 offset:1024
	ds_read_b128 v[26:29], v30 offset:2048
	ds_read_b128 v[30:33], v30 offset:3072
	s_mov_b32 m0, s87
	v_lshl_add_u64 v[216:217], s[18:19], 0, v[216:217]
	ds_read_b128 v[34:37], v225 offset:32768
	ds_read_b128 v[38:41], v225 offset:33792
	ds_read_b128 v[42:45], v225 offset:34816
	ds_read_b128 v[46:49], v225 offset:35840
	ds_read_b128 v[50:53], v225 offset:36864
	ds_read_b128 v[54:57], v225 offset:37888
	ds_read_b128 v[58:61], v225 offset:38912
	ds_read_b128 v[62:65], v225 offset:39936
	global_load_lds_dwordx4 v[216:217], off
	v_lshl_add_u64 v[214:215], s[18:19], 0, v[214:215]
	s_mov_b32 m0, s88
	s_nop 0
	global_load_lds_dwordx4 v[214:215], off
	s_waitcnt vmcnt(8)
	s_waitcnt lgkmcnt(0)
	s_barrier
	s_setprio 1
	s_waitcnt lgkmcnt(0)
	v_mfma_f32_16x16x128_f8f6f4 v[190:193], v[2:9], v[34:41], v[190:193]
	v_mfma_f32_16x16x128_f8f6f4 v[186:189], v[10:17], v[34:41], v[186:189]
	v_mfma_f32_16x16x128_f8f6f4 v[174:177], v[2:9], v[42:49], v[174:177]
	v_mfma_f32_16x16x128_f8f6f4 v[170:173], v[10:17], v[42:49], v[170:173]
	v_mfma_f32_16x16x128_f8f6f4 v[158:161], v[2:9], v[50:57], v[158:161]
	v_mfma_f32_16x16x128_f8f6f4 v[154:157], v[10:17], v[50:57], v[154:157]
	v_mfma_f32_16x16x128_f8f6f4 v[142:145], v[2:9], v[58:65], v[142:145]
	v_mfma_f32_16x16x128_f8f6f4 v[138:141], v[10:17], v[58:65], v[138:141]
	s_setprio 0
	s_setprio 1
	v_mfma_f32_16x16x128_f8f6f4 v[182:185], v[18:25], v[34:41], v[182:185]
	v_mfma_f32_16x16x128_f8f6f4 v[178:181], v[26:33], v[34:41], v[178:181]
	v_mfma_f32_16x16x128_f8f6f4 v[166:169], v[18:25], v[42:49], v[166:169]
	v_mfma_f32_16x16x128_f8f6f4 v[162:165], v[26:33], v[42:49], v[162:165]
	v_mfma_f32_16x16x128_f8f6f4 v[150:153], v[18:25], v[50:57], v[150:153]
	v_mfma_f32_16x16x128_f8f6f4 v[146:149], v[26:33], v[50:57], v[146:149]
	v_mfma_f32_16x16x128_f8f6f4 v[134:137], v[18:25], v[58:65], v[134:137]
	v_mfma_f32_16x16x128_f8f6f4 v[130:133], v[26:33], v[58:65], v[130:133]
	s_setprio 0
	s_barrier
	s_add_i32 s18, s33, s81
	v_lshl_add_u64 v[214:215], v[234:235], 0, s[34:35]
	s_mov_b32 m0, s18
	ds_read_b128 v[34:37], v225 offset:49152
	ds_read_b128 v[38:41], v225 offset:50176
	ds_read_b128 v[42:45], v225 offset:51200
	ds_read_b128 v[46:49], v225 offset:52224
	ds_read_b128 v[50:53], v225 offset:53248
	ds_read_b128 v[54:57], v225 offset:54272
	ds_read_b128 v[58:61], v225 offset:55296
	ds_read_b128 v[62:65], v225 offset:56320
	s_bitset1_b32 s28, 7
	global_load_lds_dwordx4 v[214:215], off
	s_add_i32 m0, s18, 0x2000
	s_add_u32 s16, s16, 0x40080
	v_lshl_add_u64 v[214:215], v[236:237], 0, s[34:35]
	s_addc_u32 s17, s17, 0
	s_add_i32 s18, s40, s81
	global_load_lds_dwordx4 v[214:215], off
	v_lshl_add_u64 v[214:215], s[16:17], 0, v[194:195]
	s_mov_b32 m0, s18
	s_nop 0
	global_load_lds_dwordx4 v[214:215], off
	v_lshl_add_u64 v[214:215], s[16:17], 0, v[196:197]
	s_add_i32 m0, s18, 0x2000
	s_nop 0
	global_load_lds_dwordx4 v[214:215], off
	v_lshl_add_u64 v[214:215], s[24:25], 0, v[198:199]
	v_lshl_add_u64 v[214:215], v[214:215], 0, s[28:29]
	s_mov_b32 m0, s89
	s_nop 0
	global_load_lds_dwordx4 v[214:215], off
	v_lshl_add_u64 v[214:215], s[24:25], 0, v[200:201]
	v_lshl_add_u64 v[214:215], v[214:215], 0, s[28:29]
	s_mov_b32 m0, s90
	s_nop 0
	global_load_lds_dwordx4 v[214:215], off
	s_waitcnt vmcnt(8)
	s_waitcnt lgkmcnt(0)
	s_barrier
	s_setprio 1
	s_waitcnt lgkmcnt(0)
	v_mfma_f32_16x16x128_f8f6f4 v[126:129], v[2:9], v[34:41], v[126:129]
	v_mfma_f32_16x16x128_f8f6f4 v[122:125], v[10:17], v[34:41], v[122:125]
	v_mfma_f32_16x16x128_f8f6f4 v[110:113], v[2:9], v[42:49], v[110:113]
	v_mfma_f32_16x16x128_f8f6f4 v[106:109], v[10:17], v[42:49], v[106:109]
	v_mfma_f32_16x16x128_f8f6f4 v[94:97], v[2:9], v[50:57], v[94:97]
	v_mfma_f32_16x16x128_f8f6f4 v[90:93], v[10:17], v[50:57], v[90:93]
	v_mfma_f32_16x16x128_f8f6f4 v[78:81], v[2:9], v[58:65], v[78:81]
	v_mfma_f32_16x16x128_f8f6f4 v[74:77], v[10:17], v[58:65], v[74:77]
	s_setprio 0
	s_setprio 1
	v_mfma_f32_16x16x128_f8f6f4 v[118:121], v[18:25], v[34:41], v[118:121]
	v_mfma_f32_16x16x128_f8f6f4 v[114:117], v[26:33], v[34:41], v[114:117]
	v_mfma_f32_16x16x128_f8f6f4 v[102:105], v[18:25], v[42:49], v[102:105]
	v_mfma_f32_16x16x128_f8f6f4 v[98:101], v[26:33], v[42:49], v[98:101]
	v_mfma_f32_16x16x128_f8f6f4 v[86:89], v[18:25], v[50:57], v[86:89]
	v_mfma_f32_16x16x128_f8f6f4 v[82:85], v[26:33], v[50:57], v[82:85]
	v_mfma_f32_16x16x128_f8f6f4 v[70:73], v[18:25], v[58:65], v[70:73]
	v_mfma_f32_16x16x128_f8f6f4 v[66:69], v[26:33], v[58:65], v[66:69]
	s_setprio 0
	s_barrier
	s_add_i32 s3, s3, 2
	s_add_u32 s14, s14, 0x100
	s_addc_u32 s15, s15, 0
	s_branch .LBB0_285

.LBB0_1107:
	v_lshl_add_u32 v212, s14, 8, v223
	v_lshl_or_b32 v210, s56, 8, v225
	v_mov_b32_e32 v215, v199
	v_mov_b32_e32 v217, v199
	s_mov_b32 s55, -2
	s_mov_b64 s[56:57], 0x38c00080
	v_add_u32_e32 v2, 0, v224
	v_add_u32_e32 v3, 0x10000, v2
	v_add_u32_e32 v14, 0x14000, v2
	ds_read_b128 v[18:21], v3
	ds_read_b128 v[22:25], v3 offset:1024
	ds_read_b128 v[26:29], v3 offset:2048
	ds_read_b128 v[30:33], v3 offset:3072
	ds_read_b128 v[2:5], v14
	ds_read_b128 v[6:9], v14 offset:1024
	ds_read_b128 v[10:13], v14 offset:2048
	ds_read_b128 v[14:17], v14 offset:3072
	s_cmp_eq_u32 s55, 12
	s_cselect_b64 s[58:59], -1, 0
	s_add_i32 m0, s41, 0xc000
	s_add_u32 s60, s8, s56
	s_addc_u32 s61, s9, s57
	s_add_i32 s14, s41, 0xe000
	s_cmp_lg_u32 s55, 12
	ds_read_b128 v[58:61], v226
	ds_read_b128 v[62:65], v226 offset:1024
	ds_read_b128 v[50:53], v226 offset:2048
	ds_read_b128 v[54:57], v226 offset:3072
	ds_read_b128 v[42:45], v226 offset:4096
	ds_read_b128 v[46:49], v226 offset:5120
	ds_read_b128 v[34:37], v226 offset:6144
	ds_read_b128 v[38:41], v226 offset:7168
	global_load_lds_dwordx4 v202, s[60:61]
	s_mov_b32 m0, s14
	s_nop 0
	global_load_lds_dwordx4 v204, s[60:61]
	v_mov_b32_e32 v203, v199
	v_mov_b32_e32 v205, v199
	v_mov_b64_e32 v[218:219], v[204:205]
	v_mov_b64_e32 v[220:221], v[202:203]
	s_waitcnt vmcnt(8)
	s_waitcnt lgkmcnt(0)
	s_add_i32 s14, s56, 0xc7400080
	s_and_b64 s[58:59], s[58:59], exec
	s_cselect_b32 s14, 0, s14
	s_barrier
	s_setprio 1
	s_waitcnt lgkmcnt(0)
	v_mfma_f32_16x16x128_f8f6f4 v[190:193], v[18:25], v[58:65], 0
	v_mfma_f32_16x16x128_f8f6f4 v[186:189], v[26:33], v[58:65], 0
	v_mfma_f32_16x16x128_f8f6f4 v[174:177], v[18:25], v[50:57], 0
	v_mfma_f32_16x16x128_f8f6f4 v[170:173], v[26:33], v[50:57], 0
	v_mfma_f32_16x16x128_f8f6f4 v[158:161], v[18:25], v[42:49], 0
	v_mfma_f32_16x16x128_f8f6f4 v[154:157], v[26:33], v[42:49], 0
	v_mfma_f32_16x16x128_f8f6f4 v[142:145], v[18:25], v[34:41], 0
	v_mfma_f32_16x16x128_f8f6f4 v[138:141], v[26:33], v[34:41], 0
	s_setprio 0
	s_setprio 1
	v_mfma_f32_16x16x128_f8f6f4 v[182:185], v[2:9], v[58:65], 0
	v_mfma_f32_16x16x128_f8f6f4 v[178:181], v[10:17], v[58:65], 0
	v_mfma_f32_16x16x128_f8f6f4 v[166:169], v[2:9], v[50:57], 0
	v_mfma_f32_16x16x128_f8f6f4 v[162:165], v[10:17], v[50:57], 0
	v_mfma_f32_16x16x128_f8f6f4 v[150:153], v[2:9], v[42:49], 0
	v_mfma_f32_16x16x128_f8f6f4 v[146:149], v[10:17], v[42:49], 0
	v_mfma_f32_16x16x128_f8f6f4 v[134:137], v[2:9], v[34:41], 0
	v_mfma_f32_16x16x128_f8f6f4 v[130:133], v[10:17], v[34:41], 0
	s_setprio 0
	s_barrier
	s_add_u32 s58, s12, s14
	s_addc_u32 s59, s13, 0
	s_mov_b32 m0, s42
	v_lshl_add_u64 v[228:229], s[58:59], 0, v[194:195]
	s_add_u32 s60, s58, 0x40000
	ds_read_b128 v[34:37], v226 offset:16384
	ds_read_b128 v[38:41], v226 offset:17408
	ds_read_b128 v[42:45], v226 offset:18432
	ds_read_b128 v[46:49], v226 offset:19456
	ds_read_b128 v[50:53], v226 offset:20480
	ds_read_b128 v[54:57], v226 offset:21504
	ds_read_b128 v[58:61], v226 offset:22528
	ds_read_b128 v[62:65], v226 offset:23552
	global_load_lds_dwordx4 v[228:229], off
	v_lshl_add_u64 v[230:231], s[58:59], 0, v[196:197]
	s_mov_b32 m0, s43
	s_addc_u32 s61, s59, 0
	global_load_lds_dwordx4 v[230:231], off
	v_lshl_add_u64 v[232:233], s[60:61], 0, v[194:195]
	s_mov_b32 m0, s46
	v_mov_b32_e32 v201, v199
	global_load_lds_dwordx4 v[232:233], off
	v_lshl_add_u64 v[232:233], s[60:61], 0, v[196:197]
	s_mov_b32 m0, s47
	s_add_u32 s60, s10, s14
	global_load_lds_dwordx4 v[232:233], off
	s_addc_u32 s61, s11, 0
	s_mov_b32 m0, s41
	s_nop 0
	global_load_lds_dwordx4 v198, s[60:61]
	s_mov_b32 m0, s48
	s_nop 0
	global_load_lds_dwordx4 v200, s[60:61]
	s_waitcnt vmcnt(8)
	s_waitcnt lgkmcnt(0)
	s_barrier
	s_setprio 1
	s_waitcnt lgkmcnt(0)
	v_mfma_f32_16x16x128_f8f6f4 v[126:129], v[18:25], v[34:41], 0
	v_mfma_f32_16x16x128_f8f6f4 v[122:125], v[26:33], v[34:41], 0
	v_mfma_f32_16x16x128_f8f6f4 v[110:113], v[18:25], v[42:49], 0
	v_mfma_f32_16x16x128_f8f6f4 v[106:109], v[26:33], v[42:49], 0
	v_mfma_f32_16x16x128_f8f6f4 v[94:97], v[18:25], v[50:57], 0
	v_mfma_f32_16x16x128_f8f6f4 v[90:93], v[26:33], v[50:57], 0
	v_mfma_f32_16x16x128_f8f6f4 v[78:81], v[18:25], v[58:65], 0
	v_mfma_f32_16x16x128_f8f6f4 v[74:77], v[26:33], v[58:65], 0
	s_setprio 0
	s_setprio 1
	v_mfma_f32_16x16x128_f8f6f4 v[118:121], v[2:9], v[34:41], 0
	v_mfma_f32_16x16x128_f8f6f4 v[114:117], v[10:17], v[34:41], 0
	v_mfma_f32_16x16x128_f8f6f4 v[102:105], v[2:9], v[42:49], 0
	v_mfma_f32_16x16x128_f8f6f4 v[98:101], v[10:17], v[42:49], 0
	v_mfma_f32_16x16x128_f8f6f4 v[86:89], v[2:9], v[50:57], 0
	v_mfma_f32_16x16x128_f8f6f4 v[82:85], v[10:17], v[50:57], 0
	v_mfma_f32_16x16x128_f8f6f4 v[70:73], v[2:9], v[58:65], 0
	v_mfma_f32_16x16x128_f8f6f4 v[66:69], v[10:17], v[58:65], 0
	s_setprio 0
	s_barrier
	s_add_i32 s77, 0, 0x18000
	s_add_i32 s78, 0, 0x1c000
	v_add_u32_e32 v14, s77, v224
	v_add_u32_e32 v30, s78, v224
	ds_read_b128 v[2:5], v14
	ds_read_b128 v[6:9], v14 offset:1024
	ds_read_b128 v[10:13], v14 offset:2048
	ds_read_b128 v[14:17], v14 offset:3072
	ds_read_b128 v[18:21], v30
	ds_read_b128 v[22:25], v30 offset:1024
	ds_read_b128 v[26:29], v30 offset:2048
	ds_read_b128 v[30:33], v30 offset:3072
	s_mov_b32 m0, s49
	v_lshl_add_u64 v[220:221], s[60:61], 0, v[220:221]
	ds_read_b128 v[34:37], v226 offset:32768
	ds_read_b128 v[38:41], v226 offset:33792
	ds_read_b128 v[42:45], v226 offset:34816
	ds_read_b128 v[46:49], v226 offset:35840
	ds_read_b128 v[50:53], v226 offset:36864
	ds_read_b128 v[54:57], v226 offset:37888
	ds_read_b128 v[58:61], v226 offset:38912
	ds_read_b128 v[62:65], v226 offset:39936
	global_load_lds_dwordx4 v[220:221], off
	v_lshl_add_u64 v[218:219], s[60:61], 0, v[218:219]
	s_mov_b32 m0, s62
	s_nop 0
	global_load_lds_dwordx4 v[218:219], off
	s_waitcnt vmcnt(8)
	s_waitcnt lgkmcnt(0)
	s_barrier
	s_setprio 1
	s_waitcnt lgkmcnt(0)
	v_mfma_f32_16x16x128_f8f6f4 v[190:193], v[2:9], v[34:41], v[190:193]
	v_mfma_f32_16x16x128_f8f6f4 v[186:189], v[10:17], v[34:41], v[186:189]
	v_mfma_f32_16x16x128_f8f6f4 v[174:177], v[2:9], v[42:49], v[174:177]
	v_mfma_f32_16x16x128_f8f6f4 v[170:173], v[10:17], v[42:49], v[170:173]
	v_mfma_f32_16x16x128_f8f6f4 v[158:161], v[2:9], v[50:57], v[158:161]
	v_mfma_f32_16x16x128_f8f6f4 v[154:157], v[10:17], v[50:57], v[154:157]
	v_mfma_f32_16x16x128_f8f6f4 v[142:145], v[2:9], v[58:65], v[142:145]
	v_mfma_f32_16x16x128_f8f6f4 v[138:141], v[10:17], v[58:65], v[138:141]
	s_setprio 0
	s_setprio 1
	v_mfma_f32_16x16x128_f8f6f4 v[182:185], v[18:25], v[34:41], v[182:185]
	v_mfma_f32_16x16x128_f8f6f4 v[178:181], v[26:33], v[34:41], v[178:181]
	v_mfma_f32_16x16x128_f8f6f4 v[166:169], v[18:25], v[42:49], v[166:169]
	v_mfma_f32_16x16x128_f8f6f4 v[162:165], v[26:33], v[42:49], v[162:165]
	v_mfma_f32_16x16x128_f8f6f4 v[150:153], v[18:25], v[50:57], v[150:153]
	v_mfma_f32_16x16x128_f8f6f4 v[146:149], v[26:33], v[50:57], v[146:149]
	v_mfma_f32_16x16x128_f8f6f4 v[134:137], v[18:25], v[58:65], v[134:137]
	v_mfma_f32_16x16x128_f8f6f4 v[130:133], v[26:33], v[58:65], v[130:133]
	s_setprio 0
	s_barrier
	s_add_i32 s60, s77, s40
	v_lshl_add_u64 v[218:219], v[228:229], 0, s[18:19]
	s_mov_b32 m0, s60
	ds_read_b128 v[34:37], v226 offset:49152
	ds_read_b128 v[38:41], v226 offset:50176
	ds_read_b128 v[42:45], v226 offset:51200
	ds_read_b128 v[46:49], v226 offset:52224
	ds_read_b128 v[50:53], v226 offset:53248
	ds_read_b128 v[54:57], v226 offset:54272
	ds_read_b128 v[58:61], v226 offset:55296
	ds_read_b128 v[62:65], v226 offset:56320
	s_bitset1_b32 s14, 7
	global_load_lds_dwordx4 v[218:219], off
	s_add_i32 m0, s60, 0x2000
	s_add_u32 s58, s58, 0x40080
	v_lshl_add_u64 v[218:219], v[230:231], 0, s[18:19]
	s_addc_u32 s59, s59, 0
	s_add_i32 s60, s78, s40
	global_load_lds_dwordx4 v[218:219], off
	v_lshl_add_u64 v[218:219], s[58:59], 0, v[194:195]
	s_mov_b32 m0, s60
	s_nop 0
	global_load_lds_dwordx4 v[218:219], off
	v_lshl_add_u64 v[218:219], s[58:59], 0, v[196:197]
	s_add_i32 m0, s60, 0x2000
	s_nop 0
	global_load_lds_dwordx4 v[218:219], off
	v_lshl_add_u64 v[218:219], s[10:11], 0, v[198:199]
	v_lshl_add_u64 v[218:219], v[218:219], 0, s[14:15]
	s_mov_b32 m0, s64
	s_nop 0
	global_load_lds_dwordx4 v[218:219], off
	v_lshl_add_u64 v[218:219], s[10:11], 0, v[200:201]
	v_lshl_add_u64 v[218:219], v[218:219], 0, s[14:15]
	s_mov_b32 m0, s65
	s_nop 0
	global_load_lds_dwordx4 v[218:219], off
	s_waitcnt vmcnt(8)
	s_waitcnt lgkmcnt(0)
	s_barrier
	s_setprio 1
	s_waitcnt lgkmcnt(0)
	v_mfma_f32_16x16x128_f8f6f4 v[126:129], v[2:9], v[34:41], v[126:129]
	v_mfma_f32_16x16x128_f8f6f4 v[122:125], v[10:17], v[34:41], v[122:125]
	v_mfma_f32_16x16x128_f8f6f4 v[110:113], v[2:9], v[42:49], v[110:113]
	v_mfma_f32_16x16x128_f8f6f4 v[106:109], v[10:17], v[42:49], v[106:109]
	v_mfma_f32_16x16x128_f8f6f4 v[94:97], v[2:9], v[50:57], v[94:97]
	v_mfma_f32_16x16x128_f8f6f4 v[90:93], v[10:17], v[50:57], v[90:93]
	v_mfma_f32_16x16x128_f8f6f4 v[78:81], v[2:9], v[58:65], v[78:81]
	v_mfma_f32_16x16x128_f8f6f4 v[74:77], v[10:17], v[58:65], v[74:77]
	s_setprio 0
	s_setprio 1
	v_mfma_f32_16x16x128_f8f6f4 v[118:121], v[18:25], v[34:41], v[118:121]
	v_mfma_f32_16x16x128_f8f6f4 v[114:117], v[26:33], v[34:41], v[114:117]
	v_mfma_f32_16x16x128_f8f6f4 v[102:105], v[18:25], v[42:49], v[102:105]
	v_mfma_f32_16x16x128_f8f6f4 v[98:101], v[26:33], v[42:49], v[98:101]
	v_mfma_f32_16x16x128_f8f6f4 v[86:89], v[18:25], v[50:57], v[86:89]
	v_mfma_f32_16x16x128_f8f6f4 v[82:85], v[26:33], v[50:57], v[82:85]
	v_mfma_f32_16x16x128_f8f6f4 v[70:73], v[18:25], v[58:65], v[70:73]
	v_mfma_f32_16x16x128_f8f6f4 v[66:69], v[26:33], v[58:65], v[66:69]
	s_setprio 0
	s_barrier
	s_add_i32 s55, s55, 2
	s_add_u32 s56, s56, 0x100
	s_addc_u32 s57, s57, 0
	s_branch .LBB0_1110

.LBB0_1189:
	v_mov_b32_e32 v211, v199
	v_mov_b32_e32 v213, v199
	s_mov_b32 s35, -2
	s_mov_b64 s[36:37], 0x24c00080
	ds_read_b128 v[18:21], v222
	ds_read_b128 v[22:25], v222 offset:1024
	ds_read_b128 v[26:29], v222 offset:2048
	ds_read_b128 v[30:33], v222 offset:3072
	ds_read_b128 v[2:5], v223
	ds_read_b128 v[6:9], v223 offset:1024
	ds_read_b128 v[10:13], v223 offset:2048
	ds_read_b128 v[14:17], v223 offset:3072
	s_add_i32 m0, s41, 0xc000
	s_add_u32 s38, s8, s36
	s_addc_u32 s39, s9, s37
	ds_read_b128 v[58:61], v224
	ds_read_b128 v[62:65], v224 offset:1024
	ds_read_b128 v[50:53], v224 offset:2048
	ds_read_b128 v[54:57], v224 offset:3072
	ds_read_b128 v[42:45], v224 offset:4096
	ds_read_b128 v[46:49], v224 offset:5120
	ds_read_b128 v[34:37], v224 offset:6144
	ds_read_b128 v[38:41], v224 offset:7168
	global_load_lds_dwordx4 v202, s[38:39]
	s_add_i32 m0, s41, 0xe000
	s_cmp_eq_u32 s35, 12
	global_load_lds_dwordx4 v204, s[38:39]
	s_cselect_b64 s[38:39], -1, 0
	s_cmp_lg_u32 s35, 12
	v_mov_b32_e32 v203, v199
	v_mov_b32_e32 v205, v199
	v_mov_b64_e32 v[214:215], v[204:205]
	v_mov_b64_e32 v[216:217], v[202:203]
	s_waitcnt vmcnt(8)
	s_waitcnt lgkmcnt(0)
	s_add_i32 s14, s36, 0xdb400080
	s_and_b64 s[38:39], s[38:39], exec
	s_cselect_b32 s14, 0, s14
	s_barrier
	s_setprio 1
	s_waitcnt lgkmcnt(0)
	v_mfma_f32_16x16x128_f8f6f4 v[190:193], v[18:25], v[58:65], 0
	v_mfma_f32_16x16x128_f8f6f4 v[186:189], v[26:33], v[58:65], 0
	v_mfma_f32_16x16x128_f8f6f4 v[178:181], v[18:25], v[50:57], 0
	v_mfma_f32_16x16x128_f8f6f4 v[170:173], v[26:33], v[50:57], 0
	v_mfma_f32_16x16x128_f8f6f4 v[162:165], v[18:25], v[42:49], 0
	v_mfma_f32_16x16x128_f8f6f4 v[154:157], v[26:33], v[42:49], 0
	v_mfma_f32_16x16x128_f8f6f4 v[146:149], v[18:25], v[34:41], 0
	v_mfma_f32_16x16x128_f8f6f4 v[138:141], v[26:33], v[34:41], 0
	s_setprio 0
	s_setprio 1
	v_mfma_f32_16x16x128_f8f6f4 v[182:185], v[2:9], v[58:65], 0
	v_mfma_f32_16x16x128_f8f6f4 v[174:177], v[10:17], v[58:65], 0
	v_mfma_f32_16x16x128_f8f6f4 v[166:169], v[2:9], v[50:57], 0
	v_mfma_f32_16x16x128_f8f6f4 v[158:161], v[10:17], v[50:57], 0
	v_mfma_f32_16x16x128_f8f6f4 v[150:153], v[2:9], v[42:49], 0
	v_mfma_f32_16x16x128_f8f6f4 v[142:145], v[10:17], v[42:49], 0
	v_mfma_f32_16x16x128_f8f6f4 v[134:137], v[2:9], v[34:41], 0
	v_mfma_f32_16x16x128_f8f6f4 v[130:133], v[10:17], v[34:41], 0
	s_setprio 0
	s_barrier
	s_add_u32 s38, s12, s14
	s_addc_u32 s39, s13, 0
	s_mov_b32 m0, s42
	v_lshl_add_u64 v[228:229], s[38:39], 0, v[194:195]
	s_add_u32 s50, s38, 0x40000
	ds_read_b128 v[34:37], v224 offset:16384
	ds_read_b128 v[38:41], v224 offset:17408
	ds_read_b128 v[42:45], v224 offset:18432
	ds_read_b128 v[46:49], v224 offset:19456
	ds_read_b128 v[50:53], v224 offset:20480
	ds_read_b128 v[54:57], v224 offset:21504
	ds_read_b128 v[58:61], v224 offset:22528
	ds_read_b128 v[62:65], v224 offset:23552
	global_load_lds_dwordx4 v[228:229], off
	v_lshl_add_u64 v[230:231], s[38:39], 0, v[196:197]
	s_mov_b32 m0, s43
	s_addc_u32 s51, s39, 0
	global_load_lds_dwordx4 v[230:231], off
	v_lshl_add_u64 v[232:233], s[50:51], 0, v[194:195]
	s_mov_b32 m0, s46
	v_mov_b32_e32 v201, v199
	global_load_lds_dwordx4 v[232:233], off
	v_lshl_add_u64 v[232:233], s[50:51], 0, v[196:197]
	s_mov_b32 m0, s47
	s_add_u32 s50, s10, s14
	global_load_lds_dwordx4 v[232:233], off
	s_addc_u32 s51, s11, 0
	s_mov_b32 m0, s41
	s_nop 0
	global_load_lds_dwordx4 v198, s[50:51]
	s_mov_b32 m0, s48
	s_nop 0
	global_load_lds_dwordx4 v200, s[50:51]
	s_waitcnt vmcnt(8)
	s_waitcnt lgkmcnt(0)
	s_barrier
	s_setprio 1
	s_waitcnt lgkmcnt(0)
	v_mfma_f32_16x16x128_f8f6f4 v[126:129], v[18:25], v[34:41], 0
	v_mfma_f32_16x16x128_f8f6f4 v[122:125], v[26:33], v[34:41], 0
	v_mfma_f32_16x16x128_f8f6f4 v[118:121], v[18:25], v[42:49], 0
	v_mfma_f32_16x16x128_f8f6f4 v[110:113], v[26:33], v[42:49], 0
	v_mfma_f32_16x16x128_f8f6f4 v[102:105], v[18:25], v[50:57], 0
	v_mfma_f32_16x16x128_f8f6f4 v[94:97], v[26:33], v[50:57], 0
	v_mfma_f32_16x16x128_f8f6f4 v[86:89], v[18:25], v[58:65], 0
	v_mfma_f32_16x16x128_f8f6f4 v[78:81], v[26:33], v[58:65], 0
	s_setprio 0
	s_setprio 1
	v_mfma_f32_16x16x128_f8f6f4 v[114:117], v[2:9], v[34:41], 0
	v_mfma_f32_16x16x128_f8f6f4 v[106:109], v[10:17], v[34:41], 0
	v_mfma_f32_16x16x128_f8f6f4 v[98:101], v[2:9], v[42:49], 0
	v_mfma_f32_16x16x128_f8f6f4 v[90:93], v[10:17], v[42:49], 0
	v_mfma_f32_16x16x128_f8f6f4 v[82:85], v[2:9], v[50:57], 0
	v_mfma_f32_16x16x128_f8f6f4 v[74:77], v[10:17], v[50:57], 0
	v_mfma_f32_16x16x128_f8f6f4 v[70:73], v[2:9], v[58:65], 0
	v_mfma_f32_16x16x128_f8f6f4 v[66:69], v[10:17], v[58:65], 0
	s_setprio 0
	s_barrier
	s_add_i32 s61, 0, 0x18000
	s_add_i32 s62, 0, 0x1c000
	v_add_u32_e32 v14, s61, v220
	v_add_u32_e32 v30, s62, v220
	ds_read_b128 v[2:5], v14
	ds_read_b128 v[6:9], v14 offset:1024
	ds_read_b128 v[10:13], v14 offset:2048
	ds_read_b128 v[14:17], v14 offset:3072
	ds_read_b128 v[18:21], v30
	ds_read_b128 v[22:25], v30 offset:1024
	ds_read_b128 v[26:29], v30 offset:2048
	ds_read_b128 v[30:33], v30 offset:3072
	s_mov_b32 m0, s49
	v_lshl_add_u64 v[216:217], s[50:51], 0, v[216:217]
	ds_read_b128 v[34:37], v224 offset:32768
	ds_read_b128 v[38:41], v224 offset:33792
	ds_read_b128 v[42:45], v224 offset:34816
	ds_read_b128 v[46:49], v224 offset:35840
	ds_read_b128 v[50:53], v224 offset:36864
	ds_read_b128 v[54:57], v224 offset:37888
	ds_read_b128 v[58:61], v224 offset:38912
	ds_read_b128 v[62:65], v224 offset:39936
	global_load_lds_dwordx4 v[216:217], off
	v_lshl_add_u64 v[214:215], s[50:51], 0, v[214:215]
	s_mov_b32 m0, s52
	s_nop 0
	global_load_lds_dwordx4 v[214:215], off
	s_waitcnt vmcnt(8)
	s_waitcnt lgkmcnt(0)
	s_barrier
	s_setprio 1
	s_waitcnt lgkmcnt(0)
	v_mfma_f32_16x16x128_f8f6f4 v[190:193], v[2:9], v[34:41], v[190:193]
	v_mfma_f32_16x16x128_f8f6f4 v[186:189], v[10:17], v[34:41], v[186:189]
	v_mfma_f32_16x16x128_f8f6f4 v[178:181], v[2:9], v[42:49], v[178:181]
	v_mfma_f32_16x16x128_f8f6f4 v[170:173], v[10:17], v[42:49], v[170:173]
	v_mfma_f32_16x16x128_f8f6f4 v[162:165], v[2:9], v[50:57], v[162:165]
	v_mfma_f32_16x16x128_f8f6f4 v[154:157], v[10:17], v[50:57], v[154:157]
	v_mfma_f32_16x16x128_f8f6f4 v[146:149], v[2:9], v[58:65], v[146:149]
	v_mfma_f32_16x16x128_f8f6f4 v[138:141], v[10:17], v[58:65], v[138:141]
	s_setprio 0
	s_setprio 1
	v_mfma_f32_16x16x128_f8f6f4 v[182:185], v[18:25], v[34:41], v[182:185]
	v_mfma_f32_16x16x128_f8f6f4 v[174:177], v[26:33], v[34:41], v[174:177]
	v_mfma_f32_16x16x128_f8f6f4 v[166:169], v[18:25], v[42:49], v[166:169]
	v_mfma_f32_16x16x128_f8f6f4 v[158:161], v[26:33], v[42:49], v[158:161]
	v_mfma_f32_16x16x128_f8f6f4 v[150:153], v[18:25], v[50:57], v[150:153]
	v_mfma_f32_16x16x128_f8f6f4 v[142:145], v[26:33], v[50:57], v[142:145]
	v_mfma_f32_16x16x128_f8f6f4 v[134:137], v[18:25], v[58:65], v[134:137]
	v_mfma_f32_16x16x128_f8f6f4 v[130:133], v[26:33], v[58:65], v[130:133]
	s_setprio 0
	s_barrier
	s_add_i32 s50, s61, s40
	v_lshl_add_u64 v[214:215], v[228:229], 0, s[18:19]
	s_mov_b32 m0, s50
	ds_read_b128 v[34:37], v224 offset:49152
	ds_read_b128 v[38:41], v224 offset:50176
	ds_read_b128 v[42:45], v224 offset:51200
	ds_read_b128 v[46:49], v224 offset:52224
	ds_read_b128 v[50:53], v224 offset:53248
	ds_read_b128 v[54:57], v224 offset:54272
	ds_read_b128 v[58:61], v224 offset:55296
	ds_read_b128 v[62:65], v224 offset:56320
	s_bitset1_b32 s14, 7
	global_load_lds_dwordx4 v[214:215], off
	s_add_i32 m0, s50, 0x2000
	s_add_u32 s38, s38, 0x40080
	v_lshl_add_u64 v[214:215], v[230:231], 0, s[18:19]
	s_addc_u32 s39, s39, 0
	s_add_i32 s50, s62, s40
	global_load_lds_dwordx4 v[214:215], off
	v_lshl_add_u64 v[214:215], s[38:39], 0, v[194:195]
	s_mov_b32 m0, s50
	s_nop 0
	global_load_lds_dwordx4 v[214:215], off
	v_lshl_add_u64 v[214:215], s[38:39], 0, v[196:197]
	s_add_i32 m0, s50, 0x2000
	s_nop 0
	global_load_lds_dwordx4 v[214:215], off
	v_lshl_add_u64 v[214:215], s[10:11], 0, v[198:199]
	v_lshl_add_u64 v[214:215], v[214:215], 0, s[14:15]
	s_mov_b32 m0, s53
	s_nop 0
	global_load_lds_dwordx4 v[214:215], off
	v_lshl_add_u64 v[214:215], s[10:11], 0, v[200:201]
	v_lshl_add_u64 v[214:215], v[214:215], 0, s[14:15]
	s_mov_b32 m0, s54
	s_nop 0
	global_load_lds_dwordx4 v[214:215], off
	s_waitcnt vmcnt(8)
	s_waitcnt lgkmcnt(0)
	s_barrier
	s_setprio 1
	s_waitcnt lgkmcnt(0)
	v_mfma_f32_16x16x128_f8f6f4 v[126:129], v[2:9], v[34:41], v[126:129]
	v_mfma_f32_16x16x128_f8f6f4 v[122:125], v[10:17], v[34:41], v[122:125]
	v_mfma_f32_16x16x128_f8f6f4 v[118:121], v[2:9], v[42:49], v[118:121]
	v_mfma_f32_16x16x128_f8f6f4 v[110:113], v[10:17], v[42:49], v[110:113]
	v_mfma_f32_16x16x128_f8f6f4 v[102:105], v[2:9], v[50:57], v[102:105]
	v_mfma_f32_16x16x128_f8f6f4 v[94:97], v[10:17], v[50:57], v[94:97]
	v_mfma_f32_16x16x128_f8f6f4 v[86:89], v[2:9], v[58:65], v[86:89]
	v_mfma_f32_16x16x128_f8f6f4 v[78:81], v[10:17], v[58:65], v[78:81]
	s_setprio 0
	s_setprio 1
	v_mfma_f32_16x16x128_f8f6f4 v[114:117], v[18:25], v[34:41], v[114:117]
	v_mfma_f32_16x16x128_f8f6f4 v[106:109], v[26:33], v[34:41], v[106:109]
	v_mfma_f32_16x16x128_f8f6f4 v[98:101], v[18:25], v[42:49], v[98:101]
	v_mfma_f32_16x16x128_f8f6f4 v[90:93], v[26:33], v[42:49], v[90:93]
	v_mfma_f32_16x16x128_f8f6f4 v[82:85], v[18:25], v[50:57], v[82:85]
	v_mfma_f32_16x16x128_f8f6f4 v[74:77], v[26:33], v[50:57], v[74:77]
	v_mfma_f32_16x16x128_f8f6f4 v[70:73], v[18:25], v[58:65], v[70:73]
	v_mfma_f32_16x16x128_f8f6f4 v[66:69], v[26:33], v[58:65], v[66:69]
	s_setprio 0
	s_barrier
	s_add_i32 s35, s35, 2
	s_add_u32 s36, s36, 0x100
	s_addc_u32 s37, s37, 0
	s_branch .LBB0_1192

.LBB0_1363:
	v_mov_b32_e32 v211, v197
	v_mov_b32_e32 v213, v197
	s_mov_b32 s35, -2
	s_mov_b64 s[4:5], 0x24c00080
	v_add_u32_e32 v2, 0, v228
	v_add_u32_e32 v3, 0x10000, v2
	v_add_u32_e32 v14, 0x14000, v2
	ds_read_b128 v[18:21], v3
	ds_read_b128 v[22:25], v3 offset:1024
	ds_read_b128 v[26:29], v3 offset:2048
	ds_read_b128 v[30:33], v3 offset:3072
	ds_read_b128 v[2:5], v14
	ds_read_b128 v[6:9], v14 offset:1024
	ds_read_b128 v[10:13], v14 offset:2048
	ds_read_b128 v[14:17], v14 offset:3072
	s_add_u32 s38, s6, s4
	s_mov_b32 m0, s53
	s_addc_u32 s39, s7, s5
	ds_read_b128 v[58:61], v238
	ds_read_b128 v[62:65], v238 offset:1024
	ds_read_b128 v[50:53], v238 offset:2048
	ds_read_b128 v[54:57], v238 offset:3072
	ds_read_b128 v[42:45], v238 offset:4096
	ds_read_b128 v[46:49], v238 offset:5120
	ds_read_b128 v[34:37], v238 offset:6144
	ds_read_b128 v[38:41], v238 offset:7168
	global_load_lds_dwordx4 v194, s[38:39]
	s_mov_b32 m0, s54
	s_cmp_eq_u32 s35, 12
	global_load_lds_dwordx4 v204, s[38:39]
	s_cselect_b64 s[38:39], -1, 0
	s_cmp_lg_u32 s35, 12
	v_mov_b32_e32 v195, v197
	v_mov_b32_e32 v205, v197
	v_mov_b64_e32 v[216:217], v[204:205]
	v_mov_b64_e32 v[218:219], v[194:195]
	s_waitcnt vmcnt(8)
	s_waitcnt lgkmcnt(0)
	s_add_i32 s18, s4, 0xdb400080
	s_and_b64 s[38:39], s[38:39], exec
	s_cselect_b32 s18, 0, s18
	s_barrier
	s_setprio 1
	s_waitcnt lgkmcnt(0)
	v_mfma_f32_16x16x128_f8f6f4 v[182:185], v[18:25], v[58:65], 0
	v_mfma_f32_16x16x128_f8f6f4 v[190:193], v[26:33], v[58:65], 0
	v_mfma_f32_16x16x128_f8f6f4 v[166:169], v[18:25], v[50:57], 0
	v_mfma_f32_16x16x128_f8f6f4 v[174:177], v[26:33], v[50:57], 0
	v_mfma_f32_16x16x128_f8f6f4 v[150:153], v[18:25], v[42:49], 0
	v_mfma_f32_16x16x128_f8f6f4 v[158:161], v[26:33], v[42:49], 0
	v_mfma_f32_16x16x128_f8f6f4 v[134:137], v[18:25], v[34:41], 0
	v_mfma_f32_16x16x128_f8f6f4 v[142:145], v[26:33], v[34:41], 0
	s_setprio 0
	s_setprio 1
	v_mfma_f32_16x16x128_f8f6f4 v[178:181], v[2:9], v[58:65], 0
	v_mfma_f32_16x16x128_f8f6f4 v[186:189], v[10:17], v[58:65], 0
	v_mfma_f32_16x16x128_f8f6f4 v[162:165], v[2:9], v[50:57], 0
	v_mfma_f32_16x16x128_f8f6f4 v[170:173], v[10:17], v[50:57], 0
	v_mfma_f32_16x16x128_f8f6f4 v[146:149], v[2:9], v[42:49], 0
	v_mfma_f32_16x16x128_f8f6f4 v[154:157], v[10:17], v[42:49], 0
	v_mfma_f32_16x16x128_f8f6f4 v[130:133], v[2:9], v[34:41], 0
	v_mfma_f32_16x16x128_f8f6f4 v[138:141], v[10:17], v[34:41], 0
	s_setprio 0
	s_barrier
	v_lshl_add_u64 v[246:247], v[206:207], 0, s[18:19]
	s_mov_b32 m0, s33
	v_lshl_add_u64 v[248:249], v[246:247], 0, v[200:201]
	ds_read_b128 v[34:37], v238 offset:16384
	ds_read_b128 v[38:41], v238 offset:17408
	ds_read_b128 v[42:45], v238 offset:18432
	ds_read_b128 v[46:49], v238 offset:19456
	ds_read_b128 v[50:53], v238 offset:20480
	ds_read_b128 v[54:57], v238 offset:21504
	ds_read_b128 v[58:61], v238 offset:22528
	ds_read_b128 v[62:65], v238 offset:23552
	global_load_lds_dwordx4 v[248:249], off
	v_lshl_add_u64 v[250:251], v[246:247], 0, v[202:203]
	s_mov_b32 m0, s37
	v_lshl_add_u64 v[252:253], v[246:247], 0, s[16:17]
	global_load_lds_dwordx4 v[250:251], off
	v_lshl_add_u64 v[222:223], v[252:253], 0, v[200:201]
	s_mov_b32 m0, s40
	s_add_u32 s38, s12, s18
	global_load_lds_dwordx4 v[222:223], off
	v_lshl_add_u64 v[222:223], v[252:253], 0, v[202:203]
	s_mov_b32 m0, s41
	s_addc_u32 s39, s13, 0
	global_load_lds_dwordx4 v[222:223], off
	s_mov_b32 m0, s31
	v_mov_b32_e32 v199, v197
	global_load_lds_dwordx4 v196, s[38:39]
	s_mov_b32 m0, s42
	s_nop 0
	global_load_lds_dwordx4 v198, s[38:39]
	s_waitcnt vmcnt(8)
	s_waitcnt lgkmcnt(0)
	s_barrier
	s_setprio 1
	s_waitcnt lgkmcnt(0)
	v_mfma_f32_16x16x128_f8f6f4 v[118:121], v[18:25], v[34:41], 0
	v_mfma_f32_16x16x128_f8f6f4 v[126:129], v[26:33], v[34:41], 0
	v_mfma_f32_16x16x128_f8f6f4 v[102:105], v[18:25], v[42:49], 0
	v_mfma_f32_16x16x128_f8f6f4 v[110:113], v[26:33], v[42:49], 0
	v_mfma_f32_16x16x128_f8f6f4 v[86:89], v[18:25], v[50:57], 0
	v_mfma_f32_16x16x128_f8f6f4 v[94:97], v[26:33], v[50:57], 0
	v_mfma_f32_16x16x128_f8f6f4 v[70:73], v[18:25], v[58:65], 0
	v_mfma_f32_16x16x128_f8f6f4 v[78:81], v[26:33], v[58:65], 0
	s_setprio 0
	s_setprio 1
	v_mfma_f32_16x16x128_f8f6f4 v[114:117], v[2:9], v[34:41], 0
	v_mfma_f32_16x16x128_f8f6f4 v[122:125], v[10:17], v[34:41], 0
	v_mfma_f32_16x16x128_f8f6f4 v[98:101], v[2:9], v[42:49], 0
	v_mfma_f32_16x16x128_f8f6f4 v[106:109], v[10:17], v[42:49], 0
	v_mfma_f32_16x16x128_f8f6f4 v[82:85], v[2:9], v[50:57], 0
	v_mfma_f32_16x16x128_f8f6f4 v[90:93], v[10:17], v[50:57], 0
	v_mfma_f32_16x16x128_f8f6f4 v[66:69], v[2:9], v[58:65], 0
	v_mfma_f32_16x16x128_f8f6f4 v[74:77], v[10:17], v[58:65], 0
	s_setprio 0
	s_barrier
	v_add_u32_e32 v14, s55, v228
	v_add_u32_e32 v30, s56, v228
	ds_read_b128 v[2:5], v14
	ds_read_b128 v[6:9], v14 offset:1024
	ds_read_b128 v[10:13], v14 offset:2048
	ds_read_b128 v[14:17], v14 offset:3072
	ds_read_b128 v[18:21], v30
	ds_read_b128 v[22:25], v30 offset:1024
	ds_read_b128 v[26:29], v30 offset:2048
	ds_read_b128 v[30:33], v30 offset:3072
	s_mov_b32 m0, s43
	v_lshl_add_u64 v[218:219], s[38:39], 0, v[218:219]
	ds_read_b128 v[34:37], v238 offset:32768
	ds_read_b128 v[38:41], v238 offset:33792
	ds_read_b128 v[42:45], v238 offset:34816
	ds_read_b128 v[46:49], v238 offset:35840
	ds_read_b128 v[50:53], v238 offset:36864
	ds_read_b128 v[54:57], v238 offset:37888
	ds_read_b128 v[58:61], v238 offset:38912
	ds_read_b128 v[62:65], v238 offset:39936
	global_load_lds_dwordx4 v[218:219], off
	v_lshl_add_u64 v[216:217], s[38:39], 0, v[216:217]
	s_mov_b32 m0, s46
	s_nop 0
	global_load_lds_dwordx4 v[216:217], off
	s_waitcnt vmcnt(8)
	s_waitcnt lgkmcnt(0)
	s_barrier
	s_setprio 1
	s_waitcnt lgkmcnt(0)
	v_mfma_f32_16x16x128_f8f6f4 v[182:185], v[2:9], v[34:41], v[182:185]
	v_mfma_f32_16x16x128_f8f6f4 v[190:193], v[10:17], v[34:41], v[190:193]
	v_mfma_f32_16x16x128_f8f6f4 v[166:169], v[2:9], v[42:49], v[166:169]
	v_mfma_f32_16x16x128_f8f6f4 v[174:177], v[10:17], v[42:49], v[174:177]
	v_mfma_f32_16x16x128_f8f6f4 v[150:153], v[2:9], v[50:57], v[150:153]
	v_mfma_f32_16x16x128_f8f6f4 v[158:161], v[10:17], v[50:57], v[158:161]
	v_mfma_f32_16x16x128_f8f6f4 v[134:137], v[2:9], v[58:65], v[134:137]
	v_mfma_f32_16x16x128_f8f6f4 v[142:145], v[10:17], v[58:65], v[142:145]
	s_setprio 0
	s_setprio 1
	v_mfma_f32_16x16x128_f8f6f4 v[178:181], v[18:25], v[34:41], v[178:181]
	v_mfma_f32_16x16x128_f8f6f4 v[186:189], v[26:33], v[34:41], v[186:189]
	v_mfma_f32_16x16x128_f8f6f4 v[162:165], v[18:25], v[42:49], v[162:165]
	v_mfma_f32_16x16x128_f8f6f4 v[170:173], v[26:33], v[42:49], v[170:173]
	v_mfma_f32_16x16x128_f8f6f4 v[146:149], v[18:25], v[50:57], v[146:149]
	v_mfma_f32_16x16x128_f8f6f4 v[154:157], v[26:33], v[50:57], v[154:157]
	v_mfma_f32_16x16x128_f8f6f4 v[130:133], v[18:25], v[58:65], v[130:133]
	v_mfma_f32_16x16x128_f8f6f4 v[138:141], v[26:33], v[58:65], v[138:141]
	s_setprio 0
	s_barrier
	s_mov_b32 m0, s57
	v_lshl_add_u64 v[216:217], v[248:249], 0, s[22:23]
	ds_read_b128 v[34:37], v238 offset:49152
	ds_read_b128 v[38:41], v238 offset:50176
	ds_read_b128 v[42:45], v238 offset:51200
	ds_read_b128 v[46:49], v238 offset:52224
	ds_read_b128 v[50:53], v238 offset:53248
	ds_read_b128 v[54:57], v238 offset:54272
	ds_read_b128 v[58:61], v238 offset:55296
	ds_read_b128 v[62:65], v238 offset:56320
	global_load_lds_dwordx4 v[216:217], off
	v_lshl_add_u64 v[216:217], v[250:251], 0, s[22:23]
	s_mov_b32 m0, s58
	s_bitset1_b32 s18, 7
	global_load_lds_dwordx4 v[216:217], off
	v_lshl_add_u64 v[216:217], v[246:247], 0, s[24:25]
	v_lshl_add_u64 v[218:219], v[216:217], 0, v[200:201]
	s_mov_b32 m0, s59
	v_lshl_add_u64 v[216:217], v[216:217], 0, v[202:203]
	global_load_lds_dwordx4 v[218:219], off
	s_mov_b32 m0, s60
	s_nop 0
	global_load_lds_dwordx4 v[216:217], off
	v_lshl_add_u64 v[216:217], s[12:13], 0, v[196:197]
	v_lshl_add_u64 v[216:217], v[216:217], 0, s[18:19]
	s_mov_b32 m0, s47
	s_nop 0
	global_load_lds_dwordx4 v[216:217], off
	v_lshl_add_u64 v[216:217], s[12:13], 0, v[198:199]
	v_lshl_add_u64 v[216:217], v[216:217], 0, s[18:19]
	s_mov_b32 m0, s48
	s_nop 0
	global_load_lds_dwordx4 v[216:217], off
	s_waitcnt vmcnt(8)
	s_waitcnt lgkmcnt(0)
	s_barrier
	s_setprio 1
	s_waitcnt lgkmcnt(0)
	v_mfma_f32_16x16x128_f8f6f4 v[118:121], v[2:9], v[34:41], v[118:121]
	v_mfma_f32_16x16x128_f8f6f4 v[126:129], v[10:17], v[34:41], v[126:129]
	v_mfma_f32_16x16x128_f8f6f4 v[102:105], v[2:9], v[42:49], v[102:105]
	v_mfma_f32_16x16x128_f8f6f4 v[110:113], v[10:17], v[42:49], v[110:113]
	v_mfma_f32_16x16x128_f8f6f4 v[86:89], v[2:9], v[50:57], v[86:89]
	v_mfma_f32_16x16x128_f8f6f4 v[94:97], v[10:17], v[50:57], v[94:97]
	v_mfma_f32_16x16x128_f8f6f4 v[70:73], v[2:9], v[58:65], v[70:73]
	v_mfma_f32_16x16x128_f8f6f4 v[78:81], v[10:17], v[58:65], v[78:81]
	s_setprio 0
	s_setprio 1
	v_mfma_f32_16x16x128_f8f6f4 v[114:117], v[18:25], v[34:41], v[114:117]
	v_mfma_f32_16x16x128_f8f6f4 v[122:125], v[26:33], v[34:41], v[122:125]
	v_mfma_f32_16x16x128_f8f6f4 v[98:101], v[18:25], v[42:49], v[98:101]
	v_mfma_f32_16x16x128_f8f6f4 v[106:109], v[26:33], v[42:49], v[106:109]
	v_mfma_f32_16x16x128_f8f6f4 v[82:85], v[18:25], v[50:57], v[82:85]
	v_mfma_f32_16x16x128_f8f6f4 v[90:93], v[26:33], v[50:57], v[90:93]
	v_mfma_f32_16x16x128_f8f6f4 v[66:69], v[18:25], v[58:65], v[66:69]
	v_mfma_f32_16x16x128_f8f6f4 v[74:77], v[26:33], v[58:65], v[74:77]
	s_setprio 0
	s_barrier
	s_add_i32 s35, s35, 2
	s_add_u32 s4, s4, 0x100
	s_addc_u32 s5, s5, 0
	s_branch .LBB0_1366

.LBB0_1452:
	s_cmp_lt_i32 s86, 11
	s_cselect_b64 s[6:7], -1, 0
	s_and_b64 s[0:1], s[6:7], s[0:1]
	s_andn2_b64 vcc, exec, s[0:1]
	s_cbranch_vccnz .LBB0_1498
	s_waitcnt vmcnt(0)
	v_mov_b32_e32 v1, v0
	s_load_dwordx2 s[8:9], s[44:45], 0xd8
	s_branch .LBB0_1459
	v_cmp_gt_i32_e32 vcc, 32, v1
	s_and_saveexec_b64 s[0:1], vcc
	s_cbranch_execz .LBB0_1455
	v_lshlrev_b32_e32 v2, 4, v1
	v_ashrrev_i32_e32 v3, 31, v2
	s_waitcnt lgkmcnt(0)
	v_lshl_add_u64 v[2:3], v[2:3], 2, s[8:9]
	v_add_co_u32_e32 v2, vcc, 0x8000, v2
	s_nop 1
	v_addc_co_u32_e32 v3, vcc, 0, v3, vcc
	global_load_dword v2, v[2:3], off sc1
	v_lshl_add_u32 v3, v1, 2, 0
	v_add_u32_e32 v3, 0x20000, v3
	s_waitcnt vmcnt(0)
	ds_write_b32 v3, v2

.LBB0_1471:
	v_mov_b32_e32 v211, v199
	v_mov_b32_e32 v213, v199
	s_mov_b32 s29, -2
	s_mov_b64 s[4:5], 0x2cc00080
	v_add_u32_e32 v2, 0, v226
	v_add_u32_e32 v3, 0x10000, v2
	v_add_u32_e32 v14, 0x14000, v2
	ds_read_b128 v[18:21], v3
	ds_read_b128 v[22:25], v3 offset:1024
	ds_read_b128 v[26:29], v3 offset:2048
	ds_read_b128 v[30:33], v3 offset:3072
	ds_read_b128 v[2:5], v14
	ds_read_b128 v[6:9], v14 offset:1024
	ds_read_b128 v[10:13], v14 offset:2048
	ds_read_b128 v[14:17], v14 offset:3072
	s_add_u32 s34, s8, s4
	s_mov_b32 m0, s50
	s_addc_u32 s35, s9, s5
	ds_read_b128 v[58:61], v236
	ds_read_b128 v[62:65], v236 offset:1024
	ds_read_b128 v[50:53], v236 offset:2048
	ds_read_b128 v[54:57], v236 offset:3072
	ds_read_b128 v[42:45], v236 offset:4096
	ds_read_b128 v[46:49], v236 offset:5120
	ds_read_b128 v[34:37], v236 offset:6144
	ds_read_b128 v[38:41], v236 offset:7168
	global_load_lds_dwordx4 v202, s[34:35]
	s_mov_b32 m0, s51
	s_cmp_eq_u32 s29, 4
	global_load_lds_dwordx4 v204, s[34:35]
	s_cselect_b64 s[34:35], -1, 0
	s_cmp_lg_u32 s29, 4
	v_mov_b32_e32 v203, v199
	v_mov_b32_e32 v205, v199
	v_mov_b64_e32 v[216:217], v[204:205]
	v_mov_b64_e32 v[218:219], v[202:203]
	s_waitcnt vmcnt(8)
	s_waitcnt lgkmcnt(0)
	s_add_i32 s16, s4, 0xd3400080
	s_and_b64 s[34:35], s[34:35], exec
	s_cselect_b32 s16, 0, s16
	s_barrier
	s_setprio 1
	s_waitcnt lgkmcnt(0)
	v_mfma_f32_16x16x128_f8f6f4 v[190:193], v[18:25], v[58:65], 0
	v_mfma_f32_16x16x128_f8f6f4 v[186:189], v[26:33], v[58:65], 0
	v_mfma_f32_16x16x128_f8f6f4 v[178:181], v[18:25], v[50:57], 0
	v_mfma_f32_16x16x128_f8f6f4 v[170:173], v[26:33], v[50:57], 0
	v_mfma_f32_16x16x128_f8f6f4 v[162:165], v[18:25], v[42:49], 0
	v_mfma_f32_16x16x128_f8f6f4 v[154:157], v[26:33], v[42:49], 0
	v_mfma_f32_16x16x128_f8f6f4 v[146:149], v[18:25], v[34:41], 0
	v_mfma_f32_16x16x128_f8f6f4 v[138:141], v[26:33], v[34:41], 0
	s_setprio 0
	s_setprio 1
	v_mfma_f32_16x16x128_f8f6f4 v[182:185], v[2:9], v[58:65], 0
	v_mfma_f32_16x16x128_f8f6f4 v[174:177], v[10:17], v[58:65], 0
	v_mfma_f32_16x16x128_f8f6f4 v[166:169], v[2:9], v[50:57], 0
	v_mfma_f32_16x16x128_f8f6f4 v[158:161], v[10:17], v[50:57], 0
	v_mfma_f32_16x16x128_f8f6f4 v[150:153], v[2:9], v[42:49], 0
	v_mfma_f32_16x16x128_f8f6f4 v[142:145], v[10:17], v[42:49], 0
	v_mfma_f32_16x16x128_f8f6f4 v[134:137], v[2:9], v[34:41], 0
	v_mfma_f32_16x16x128_f8f6f4 v[130:133], v[10:17], v[34:41], 0
	s_setprio 0
	s_barrier
	v_lshl_add_u64 v[242:243], v[206:207], 0, s[16:17]
	s_mov_b32 m0, s33
	v_lshl_add_u64 v[244:245], v[242:243], 0, v[194:195]
	ds_read_b128 v[34:37], v236 offset:16384
	ds_read_b128 v[38:41], v236 offset:17408
	ds_read_b128 v[42:45], v236 offset:18432
	ds_read_b128 v[46:49], v236 offset:19456
	ds_read_b128 v[50:53], v236 offset:20480
	ds_read_b128 v[54:57], v236 offset:21504
	ds_read_b128 v[58:61], v236 offset:22528
	ds_read_b128 v[62:65], v236 offset:23552
	global_load_lds_dwordx4 v[244:245], off
	v_lshl_add_u64 v[246:247], v[242:243], 0, v[196:197]
	s_mov_b32 m0, s36
	v_lshl_add_u64 v[248:249], v[242:243], 0, s[14:15]
	global_load_lds_dwordx4 v[246:247], off
	v_lshl_add_u64 v[250:251], v[248:249], 0, v[194:195]
	s_mov_b32 m0, s37
	v_lshl_add_u64 v[248:249], v[248:249], 0, v[196:197]
	global_load_lds_dwordx4 v[250:251], off
	s_mov_b32 m0, s38
	s_add_u32 s34, s10, s16
	global_load_lds_dwordx4 v[248:249], off
	s_addc_u32 s35, s11, 0
	s_mov_b32 m0, s31
	v_mov_b32_e32 v201, v199
	global_load_lds_dwordx4 v198, s[34:35]
	s_mov_b32 m0, s39
	s_nop 0
	global_load_lds_dwordx4 v200, s[34:35]
	s_waitcnt vmcnt(8)
	s_waitcnt lgkmcnt(0)
	s_barrier
	s_setprio 1
	s_waitcnt lgkmcnt(0)
	v_mfma_f32_16x16x128_f8f6f4 v[126:129], v[18:25], v[34:41], 0
	v_mfma_f32_16x16x128_f8f6f4 v[122:125], v[26:33], v[34:41], 0
	v_mfma_f32_16x16x128_f8f6f4 v[114:117], v[18:25], v[42:49], 0
	v_mfma_f32_16x16x128_f8f6f4 v[106:109], v[26:33], v[42:49], 0
	v_mfma_f32_16x16x128_f8f6f4 v[98:101], v[18:25], v[50:57], 0
	v_mfma_f32_16x16x128_f8f6f4 v[90:93], v[26:33], v[50:57], 0
	v_mfma_f32_16x16x128_f8f6f4 v[82:85], v[18:25], v[58:65], 0
	v_mfma_f32_16x16x128_f8f6f4 v[74:77], v[26:33], v[58:65], 0
	s_setprio 0
	s_setprio 1
	v_mfma_f32_16x16x128_f8f6f4 v[118:121], v[2:9], v[34:41], 0
	v_mfma_f32_16x16x128_f8f6f4 v[110:113], v[10:17], v[34:41], 0
	v_mfma_f32_16x16x128_f8f6f4 v[102:105], v[2:9], v[42:49], 0
	v_mfma_f32_16x16x128_f8f6f4 v[94:97], v[10:17], v[42:49], 0
	v_mfma_f32_16x16x128_f8f6f4 v[86:89], v[2:9], v[50:57], 0
	v_mfma_f32_16x16x128_f8f6f4 v[78:81], v[10:17], v[50:57], 0
	v_mfma_f32_16x16x128_f8f6f4 v[70:73], v[2:9], v[58:65], 0
	v_mfma_f32_16x16x128_f8f6f4 v[66:69], v[10:17], v[58:65], 0
	s_setprio 0
	s_barrier
	v_add_u32_e32 v14, s52, v226
	v_add_u32_e32 v30, s53, v226
	ds_read_b128 v[2:5], v14
	ds_read_b128 v[6:9], v14 offset:1024
	ds_read_b128 v[10:13], v14 offset:2048
	ds_read_b128 v[14:17], v14 offset:3072
	ds_read_b128 v[18:21], v30
	ds_read_b128 v[22:25], v30 offset:1024
	ds_read_b128 v[26:29], v30 offset:2048
	ds_read_b128 v[30:33], v30 offset:3072
	s_mov_b32 m0, s40
	v_lshl_add_u64 v[218:219], s[34:35], 0, v[218:219]
	ds_read_b128 v[34:37], v236 offset:32768
	ds_read_b128 v[38:41], v236 offset:33792
	ds_read_b128 v[42:45], v236 offset:34816
	ds_read_b128 v[46:49], v236 offset:35840
	ds_read_b128 v[50:53], v236 offset:36864
	ds_read_b128 v[54:57], v236 offset:37888
	ds_read_b128 v[58:61], v236 offset:38912
	ds_read_b128 v[62:65], v236 offset:39936
	global_load_lds_dwordx4 v[218:219], off
	v_lshl_add_u64 v[216:217], s[34:35], 0, v[216:217]
	s_mov_b32 m0, s41
	s_nop 0
	global_load_lds_dwordx4 v[216:217], off
	s_waitcnt vmcnt(8)
	s_waitcnt lgkmcnt(0)
	s_barrier
	s_setprio 1
	s_waitcnt lgkmcnt(0)
	v_mfma_f32_16x16x128_f8f6f4 v[190:193], v[2:9], v[34:41], v[190:193]
	v_mfma_f32_16x16x128_f8f6f4 v[186:189], v[10:17], v[34:41], v[186:189]
	v_mfma_f32_16x16x128_f8f6f4 v[178:181], v[2:9], v[42:49], v[178:181]
	v_mfma_f32_16x16x128_f8f6f4 v[170:173], v[10:17], v[42:49], v[170:173]
	v_mfma_f32_16x16x128_f8f6f4 v[162:165], v[2:9], v[50:57], v[162:165]
	v_mfma_f32_16x16x128_f8f6f4 v[154:157], v[10:17], v[50:57], v[154:157]
	v_mfma_f32_16x16x128_f8f6f4 v[146:149], v[2:9], v[58:65], v[146:149]
	v_mfma_f32_16x16x128_f8f6f4 v[138:141], v[10:17], v[58:65], v[138:141]
	s_setprio 0
	s_setprio 1
	v_mfma_f32_16x16x128_f8f6f4 v[182:185], v[18:25], v[34:41], v[182:185]
	v_mfma_f32_16x16x128_f8f6f4 v[174:177], v[26:33], v[34:41], v[174:177]
	v_mfma_f32_16x16x128_f8f6f4 v[166:169], v[18:25], v[42:49], v[166:169]
	v_mfma_f32_16x16x128_f8f6f4 v[158:161], v[26:33], v[42:49], v[158:161]
	v_mfma_f32_16x16x128_f8f6f4 v[150:153], v[18:25], v[50:57], v[150:153]
	v_mfma_f32_16x16x128_f8f6f4 v[142:145], v[26:33], v[50:57], v[142:145]
	v_mfma_f32_16x16x128_f8f6f4 v[134:137], v[18:25], v[58:65], v[134:137]
	v_mfma_f32_16x16x128_f8f6f4 v[130:133], v[26:33], v[58:65], v[130:133]
	s_setprio 0
	s_barrier
	s_mov_b32 m0, s54
	v_lshl_add_u64 v[216:217], v[244:245], 0, s[20:21]
	ds_read_b128 v[34:37], v236 offset:49152
	ds_read_b128 v[38:41], v236 offset:50176
	ds_read_b128 v[42:45], v236 offset:51200
	ds_read_b128 v[46:49], v236 offset:52224
	ds_read_b128 v[50:53], v236 offset:53248
	ds_read_b128 v[54:57], v236 offset:54272
	ds_read_b128 v[58:61], v236 offset:55296
	ds_read_b128 v[62:65], v236 offset:56320
	global_load_lds_dwordx4 v[216:217], off
	v_lshl_add_u64 v[216:217], v[246:247], 0, s[20:21]
	s_mov_b32 m0, s55
	s_bitset1_b32 s16, 7
	global_load_lds_dwordx4 v[216:217], off
	v_lshl_add_u64 v[216:217], v[242:243], 0, s[22:23]
	v_lshl_add_u64 v[218:219], v[216:217], 0, v[194:195]
	s_mov_b32 m0, s56
	v_lshl_add_u64 v[216:217], v[216:217], 0, v[196:197]
	global_load_lds_dwordx4 v[218:219], off
	s_mov_b32 m0, s57
	s_nop 0
	global_load_lds_dwordx4 v[216:217], off
	v_lshl_add_u64 v[216:217], s[10:11], 0, v[198:199]
	v_lshl_add_u64 v[216:217], v[216:217], 0, s[16:17]
	s_mov_b32 m0, s42
	s_nop 0
	global_load_lds_dwordx4 v[216:217], off
	v_lshl_add_u64 v[216:217], s[10:11], 0, v[200:201]
	v_lshl_add_u64 v[216:217], v[216:217], 0, s[16:17]
	s_mov_b32 m0, s43
	s_nop 0
	global_load_lds_dwordx4 v[216:217], off
	s_waitcnt vmcnt(8)
	s_waitcnt lgkmcnt(0)
	s_barrier
	s_setprio 1
	s_waitcnt lgkmcnt(0)
	v_mfma_f32_16x16x128_f8f6f4 v[126:129], v[2:9], v[34:41], v[126:129]
	v_mfma_f32_16x16x128_f8f6f4 v[122:125], v[10:17], v[34:41], v[122:125]
	v_mfma_f32_16x16x128_f8f6f4 v[114:117], v[2:9], v[42:49], v[114:117]
	v_mfma_f32_16x16x128_f8f6f4 v[106:109], v[10:17], v[42:49], v[106:109]
	v_mfma_f32_16x16x128_f8f6f4 v[98:101], v[2:9], v[50:57], v[98:101]
	v_mfma_f32_16x16x128_f8f6f4 v[90:93], v[10:17], v[50:57], v[90:93]
	v_mfma_f32_16x16x128_f8f6f4 v[82:85], v[2:9], v[58:65], v[82:85]
	v_mfma_f32_16x16x128_f8f6f4 v[74:77], v[10:17], v[58:65], v[74:77]
	s_setprio 0
	s_setprio 1
	v_mfma_f32_16x16x128_f8f6f4 v[118:121], v[18:25], v[34:41], v[118:121]
	v_mfma_f32_16x16x128_f8f6f4 v[110:113], v[26:33], v[34:41], v[110:113]
	v_mfma_f32_16x16x128_f8f6f4 v[102:105], v[18:25], v[42:49], v[102:105]
	v_mfma_f32_16x16x128_f8f6f4 v[94:97], v[26:33], v[42:49], v[94:97]
	v_mfma_f32_16x16x128_f8f6f4 v[86:89], v[18:25], v[50:57], v[86:89]
	v_mfma_f32_16x16x128_f8f6f4 v[78:81], v[26:33], v[50:57], v[78:81]
	v_mfma_f32_16x16x128_f8f6f4 v[70:73], v[18:25], v[58:65], v[70:73]
	v_mfma_f32_16x16x128_f8f6f4 v[66:69], v[26:33], v[58:65], v[66:69]
	s_setprio 0
	s_barrier
	s_add_i32 s29, s29, 2
	s_add_u32 s4, s4, 0x100
	s_addc_u32 s5, s5, 0
	s_branch .LBB0_1474

.LBB0_1548:
	s_cmp_gt_i32 s86, 11
	s_cselect_b64 s[2:3], -1, 0
	s_xor_b64 s[0:1], s[0:1], -1
	s_or_b64 s[0:1], s[2:3], s[0:1]
	s_and_b64 vcc, exec, s[0:1]
	s_cbranch_vccnz .LBB0_1558
	s_load_dwordx4 s[4:7], s[44:45], 0xd0
	s_load_dwordx2 s[8:9], s[44:45], 0x38
	v_readfirstlane_b32 s2, v0
	s_branch .Lfin_tabdone
	v_cmp_gt_i32_e32 vcc, 32, v0
	s_and_saveexec_b64 s[0:1], vcc
	s_cbranch_execz .LBB0_1551
	v_lshlrev_b32_e32 v2, 4, v0
	v_ashrrev_i32_e32 v3, 31, v2
	s_waitcnt lgkmcnt(0)
	v_lshl_add_u64 v[2:3], v[2:3], 2, s[6:7]
	v_add_co_u32_e32 v2, vcc, 0x8000, v2
	s_nop 1
	v_addc_co_u32_e32 v3, vcc, 0, v3, vcc
	global_load_dword v1, v[2:3], off sc1
	v_lshl_add_u32 v2, v0, 2, 0
	s_waitcnt vmcnt(0)
	ds_write_b32 v2, v1

.Lfin_tabdone:
	s_ashr_i32 s0, s2, 6
	s_lshl_b32 s1, s94, 3
	s_add_i32 s17, s0, s1
	s_cmpk_gt_i32 s17, 0x1fff
	s_waitcnt lgkmcnt(0)
	s_barrier
	s_cbranch_scc1 .LBB0_1558
	s_add_u32 s18, s6, 0x1cc00000
	s_addc_u32 s19, s7, 0
	s_add_u32 s10, s6, 0x31c00000
	s_addc_u32 s11, s7, 0
	s_add_u32 s20, s6, 0xa00000
	s_addc_u32 s21, s7, 0
	s_add_u32 s22, s6, 0x500000
	s_addc_u32 s23, s7, 0
	s_add_u32 s24, s6, 0x540000
	s_addc_u32 s25, s7, 0
	s_add_u32 s6, s6, 0x800000
	s_addc_u32 s7, s7, 0
	v_and_b32_e32 v182, 63, v0
	s_lshl_b32 s1, s94, 5
	s_lshl_b32 s2, s0, 2
	v_mbcnt_lo_u32_b32 v0, -1, 0
	s_add_i32 s1, s1, s2
	v_mbcnt_hi_u32_b32 v184, -1, v0
	s_or_b32 s12, s1, 3
	s_lshl_b32 s1, s94, 4
	s_lshl_b32 s0, s0, 1
	v_and_b32_e32 v0, 64, v184
	s_lshl_b32 s26, s97, 3
	s_lshl_b32 s27, s97, 5
	s_add_i32 s14, s1, s0
	s_lshl_b32 s28, s97, 4
	v_mov_b32_e32 v183, 0
	s_movk_i32 s29, 0x1000
	v_add_u32_e32 v185, 64, v0
	v_xor_b32_e32 v189, 8, v184
	v_xor_b32_e32 v190, 16, v184
	v_xor_b32_e32 v191, 32, v184
	s_mov_b32 s16, 0x3e000000
	v_mov_b32_e32 v192, 0x358637bd
	s_mov_b32 s30, 0xf800000
	v_mov_b32_e32 v193, 0x260
.LBB0_1557:
	s_ashr_i32 s1, s17, 31
	s_lshr_b32 s2, s1, 22
	v_xor_b32_e32 v1, 1, v184
	s_add_i32 s2, s17, s2
	v_cmp_lt_i32_e32 vcc, v1, v185
	v_xor_b32_e32 v2, 2, v184
	s_lshr_b32 s2, s2, 10
	v_mov_b32_e32 v0, v182
	s_add_i32 s0, s12, -3
	v_cndmask_b32_e32 v1, v184, v1, vcc
	v_cmp_lt_i32_e32 vcc, v2, v185
	v_xor_b32_e32 v3, 4, v184
	s_mulk_i32 s2, 0x3000
	v_cndmask_b32_e32 v2, v184, v2, vcc
	v_cmp_lt_i32_e32 vcc, v3, v185
	s_ashr_i32 s1, s0, 31
	v_lshlrev_b32_e32 v64, 2, v0
	s_addk_i32 s2, 0x2800
	v_cndmask_b32_e32 v3, v184, v3, vcc
	v_cmp_lt_i32_e32 vcc, v189, v185
	s_lshl_b64 s[0:1], s[0:1], 2
	v_ashrrev_i32_e32 v65, 31, v64
	s_ashr_i32 s3, s2, 31
	v_cndmask_b32_e32 v4, v184, v189, vcc
	v_cmp_lt_i32_e32 vcc, v190, v185
	v_lshlrev_b64 v[98:99], 2, v[64:65]
	s_add_u32 s34, s22, s0
	v_cndmask_b32_e32 v5, v184, v190, vcc
	v_cmp_lt_i32_e32 vcc, v191, v185
	v_lshlrev_b32_e32 v199, 2, v1
	v_lshl_add_u64 v[0:1], s[8:9], 0, v[98:99]
	s_addc_u32 s35, s23, s1
	v_cndmask_b32_e32 v6, v184, v191, vcc
	v_add_co_u32_e32 v34, vcc, s29, v0
	s_add_u32 s0, s24, s0
	s_nop 0
	v_addc_co_u32_e32 v35, vcc, 0, v1, vcc
	s_addc_u32 s1, s25, s1
	v_lshlrev_b32_e32 v198, 2, v2
	v_lshlrev_b32_e32 v197, 2, v3
	v_lshlrev_b32_e32 v196, 2, v4
	v_lshlrev_b32_e32 v195, 2, v5
	v_lshlrev_b32_e32 v194, 2, v6
	global_load_dwordx4 v[28:31], v[0:1], off
	global_load_dwordx4 v[20:23], v[0:1], off offset:1024
	global_load_dwordx4 v[12:15], v[0:1], off offset:2048
	global_load_dwordx4 v[4:7], v[0:1], off offset:3072
	global_load_dwordx4 v[24:27], v[34:35], off
	global_load_dwordx4 v[16:19], v[34:35], off offset:1024
	global_load_dwordx4 v[8:11], v[34:35], off offset:2048
	s_nop 0
	global_load_dwordx4 v[0:3], v[34:35], off offset:3072
	global_load_dword v111, v183, s[34:35]
	global_load_dword v109, v183, s[0:1]
	s_add_i32 s34, s12, -2
	s_ashr_i32 s35, s34, 31
	s_lshl_b64 s[0:1], s[34:35], 2
	s_add_u32 s34, s22, s0
	s_addc_u32 s35, s23, s1
	s_add_u32 s0, s24, s0
	s_addc_u32 s1, s25, s1
	global_load_dword v112, v183, s[34:35]
	global_load_dword v107, v183, s[0:1]
	s_add_i32 s34, s12, -1
	s_ashr_i32 s35, s34, 31
	s_lshl_b64 s[0:1], s[34:35], 2
	s_add_u32 s34, s22, s0
	s_addc_u32 s35, s23, s1
	s_add_u32 s0, s24, s0
	s_addc_u32 s1, s25, s1
	s_ashr_i32 s13, s12, 31
	global_load_dword v110, v183, s[34:35]
	global_load_dword v106, v183, s[0:1]
	s_lshl_b64 s[0:1], s[12:13], 2
	s_add_u32 s34, s22, s0
	s_addc_u32 s35, s23, s1
	global_load_dword v108, v183, s[34:35]
	s_add_u32 s0, s24, s0
	s_addc_u32 s1, s25, s1
	global_load_dword v138, v183, s[0:1]
	s_ashr_i32 s15, s14, 31
	s_lshl_b64 s[0:1], s[14:15], 12
	s_add_u32 s34, s18, s0
	v_lshlrev_b64 v[32:33], 1, v[64:65]
	s_addc_u32 s35, s19, s1
	v_lshl_add_u64 v[34:35], s[34:35], 0, v[32:33]
	global_load_dwordx2 v[96:97], v[34:35], off
	global_load_dwordx2 v[94:95], v[34:35], off offset:512
	global_load_dwordx2 v[92:93], v[34:35], off offset:1024
	global_load_dwordx2 v[90:91], v[34:35], off offset:1536
	global_load_dwordx2 v[88:89], v[34:35], off offset:2048
	global_load_dwordx2 v[86:87], v[34:35], off offset:2560
	global_load_dwordx2 v[84:85], v[34:35], off offset:3072
	global_load_dwordx2 v[82:83], v[34:35], off offset:3584
	s_add_i32 s0, s14, 1
	s_ashr_i32 s1, s0, 31
	s_lshl_b64 s[34:35], s[0:1], 12
	s_add_u32 s34, s18, s34
	s_addc_u32 s35, s19, s35
	s_lshl_b64 s[2:3], s[2:3], 2
	s_add_u32 s2, s20, s2
	s_addc_u32 s3, s21, s3
	v_lshl_add_u64 v[48:49], s[2:3], 0, v[98:99]
	v_add_co_u32_e32 v100, vcc, s29, v48
	v_lshl_add_u64 v[32:33], s[34:35], 0, v[32:33]
	s_nop 0
	v_addc_co_u32_e32 v101, vcc, 0, v49, vcc
	global_load_dwordx2 v[80:81], v[32:33], off
	global_load_dwordx2 v[78:79], v[32:33], off offset:512
	global_load_dwordx2 v[76:77], v[32:33], off offset:1024
	global_load_dwordx2 v[74:75], v[32:33], off offset:1536
	global_load_dwordx2 v[72:73], v[32:33], off offset:2048
	global_load_dwordx2 v[70:71], v[32:33], off offset:2560
	global_load_dwordx2 v[68:69], v[32:33], off offset:3072
	global_load_dwordx2 v[66:67], v[32:33], off offset:3584
	global_load_dwordx4 v[44:47], v[48:49], off
	global_load_dwordx4 v[40:43], v[48:49], off offset:1024
	global_load_dwordx4 v[36:39], v[48:49], off offset:2048
	s_nop 0
	global_load_dwordx4 v[32:35], v[48:49], off offset:3072
	global_load_dwordx4 v[60:63], v[100:101], off
	global_load_dwordx4 v[56:59], v[100:101], off offset:1024
	global_load_dwordx4 v[52:55], v[100:101], off offset:2048
	s_nop 0
	global_load_dwordx4 v[48:51], v[100:101], off offset:3072
	s_lshl_b64 s[34:35], s[14:15], 13
	s_add_u32 s2, s4, s34
	s_addc_u32 s3, s5, s35
	s_lshl_b64 s[0:1], s[0:1], 13
	s_add_u32 s0, s4, s0
	s_addc_u32 s1, s5, s1
	s_add_i32 s17, s17, s26
	v_lshl_add_u64 v[100:101], s[2:3], 0, v[98:99]
	v_add_co_u32_e32 v102, vcc, s29, v100
	v_lshl_add_u64 v[104:105], s[0:1], 0, v[98:99]
	s_nop 0
	v_addc_co_u32_e32 v103, vcc, 0, v101, vcc
	v_add_co_u32_e32 v98, vcc, s29, v104
	s_add_i32 s12, s12, s27
	s_nop 0
	v_addc_co_u32_e32 v99, vcc, 0, v105, vcc
	s_add_i32 s14, s14, s28
	s_cmpk_lt_i32 s17, 0x2000
	s_waitcnt vmcnt(31)
	v_lshlrev_b32_e32 v113, 2, v111
	v_lshlrev_b32_e32 v111, 14, v111
	v_add_u32_e32 v113, 0x20000, v113
	ds_read_b32 v113, v113 offset:128
	s_waitcnt vmcnt(30)
	v_add_u32_e32 v114, v111, v109
	v_ashrrev_i32_e32 v115, 31, v114
	v_lshlrev_b64 v[114:115], 2, v[114:115]
	v_lshl_add_u64 v[114:115], s[6:7], 0, v[114:115]
	global_load_dword v140, v[114:115], off
	s_waitcnt vmcnt(30)
	v_lshlrev_b32_e32 v111, 2, v112
	v_lshlrev_b32_e32 v114, 14, v112
	v_add_u32_e32 v111, 0x20000, v111
	ds_read_b32 v116, v111 offset:128
	s_waitcnt lgkmcnt(1)
	v_add_u32_e32 v112, v113, v109
	s_waitcnt vmcnt(29)
	v_add_u32_e32 v114, v114, v107
	v_ashrrev_i32_e32 v115, 31, v114
	v_ashrrev_i32_e32 v113, 31, v112
	v_lshlrev_b64 v[114:115], 2, v[114:115]
	v_lshlrev_b64 v[112:113], 11, v[112:113]
	v_lshl_add_u64 v[114:115], s[6:7], 0, v[114:115]
	v_lshl_add_u64 v[112:113], s[10:11], 0, v[112:113]
	global_load_dword v141, v[114:115], off
	s_waitcnt vmcnt(29)
	v_lshlrev_b32_e32 v109, 2, v110
	v_lshlrev_b32_e32 v114, 14, v110
	v_lshl_add_u64 v[110:111], v[112:113], 0, v[64:65]
	global_load_dword v146, v[110:111], off
	global_load_dword v147, v[110:111], off offset:256
	global_load_dword v148, v[110:111], off offset:512
	global_load_dword v152, v[110:111], off offset:768
	global_load_dword v158, v[110:111], off offset:1024
	global_load_dword v162, v[110:111], off offset:1280
	global_load_dword v166, v[110:111], off offset:1536
	global_load_dword v168, v[110:111], off offset:1792
	s_waitcnt lgkmcnt(0)
	v_add_u32_e32 v110, v116, v107
	s_waitcnt vmcnt(36)
	v_add_u32_e32 v112, v114, v106
	v_ashrrev_i32_e32 v111, 31, v110
	s_waitcnt vmcnt(35)
	v_lshlrev_b32_e32 v107, 2, v108
	v_add_u32_e32 v109, 0x20000, v109
	v_ashrrev_i32_e32 v113, 31, v112
	v_lshlrev_b64 v[110:111], 11, v[110:111]
	v_add_u32_e32 v107, 0x20000, v107
	ds_read_b32 v115, v109 offset:128
	ds_read_b32 v139, v107 offset:128
	v_lshlrev_b64 v[112:113], 2, v[112:113]
	v_lshlrev_b32_e32 v114, 14, v108
	v_lshl_add_u64 v[108:109], s[10:11], 0, v[110:111]
	v_lshl_add_u64 v[112:113], s[6:7], 0, v[112:113]
	v_lshl_add_u64 v[108:109], v[108:109], 0, v[64:65]
	global_load_dword v142, v[112:113], off
	global_load_dword v172, v[108:109], off
	global_load_dword v174, v[108:109], off offset:256
	global_load_dword v178, v[108:109], off offset:512
	global_load_dword v180, v[108:109], off offset:768
	global_load_dword v206, v[108:109], off offset:1024
	global_load_dword v224, v[108:109], off offset:1280
	global_load_dword v228, v[108:109], off offset:1536
	global_load_dword v232, v[108:109], off offset:1792
	s_waitcnt vmcnt(43)
	v_add_u32_e32 v110, v114, v138
	v_ashrrev_i32_e32 v111, 31, v110
	v_lshlrev_b64 v[108:109], 2, v[110:111]
	v_lshl_add_u64 v[108:109], s[6:7], 0, v[108:109]
	global_load_dword v143, v[108:109], off
	s_waitcnt lgkmcnt(1)
	v_add_u32_e32 v106, v115, v106
	s_waitcnt vmcnt(36)
	v_lshlrev_b32_e32 v132, 16, v82
	v_and_b32_e32 v133, 0xffff0000, v82
	s_waitcnt lgkmcnt(0)
	v_add_u32_e32 v82, v139, v138
	v_ashrrev_i32_e32 v107, 31, v106
	v_lshlrev_b32_e32 v136, 16, v83
	v_and_b32_e32 v137, 0xffff0000, v83
	v_ashrrev_i32_e32 v83, 31, v82
	v_lshlrev_b64 v[106:107], 11, v[106:107]
	v_lshlrev_b64 v[82:83], 11, v[82:83]
	v_lshl_add_u64 v[106:107], s[10:11], 0, v[106:107]
	v_lshl_add_u64 v[138:139], s[10:11], 0, v[82:83]
	v_lshl_add_u64 v[144:145], v[106:107], 0, v[64:65]
	v_lshl_add_u64 v[64:65], v[138:139], 0, v[64:65]
	global_load_dword v238, v[144:145], off
	global_load_dword v239, v[144:145], off offset:256
	global_load_dword v240, v[144:145], off offset:512
	global_load_dword v241, v[144:145], off offset:768
	global_load_dword v242, v[144:145], off offset:1024
	global_load_dword v244, v[144:145], off offset:1280
	global_load_dword v245, v[144:145], off offset:1536
	global_load_dword v254, v[144:145], off offset:1792
	global_load_dword v186, v[64:65], off
	global_load_dword v248, v[64:65], off offset:256
	global_load_dword v249, v[64:65], off offset:512
	global_load_dword v250, v[64:65], off offset:768
	global_load_dword v187, v[64:65], off offset:1024
	global_load_dword v251, v[64:65], off offset:1280
	global_load_dword v252, v[64:65], off offset:1536
	global_load_dword v188, v[64:65], off offset:1792
	v_lshlrev_b32_e32 v106, 16, v96
	v_and_b32_e32 v107, 0xffff0000, v96
	v_lshlrev_b32_e32 v110, 16, v97
	v_and_b32_e32 v111, 0xffff0000, v97
	v_lshlrev_b32_e32 v108, 16, v94
	v_and_b32_e32 v109, 0xffff0000, v94
	v_lshlrev_b32_e32 v114, 16, v95
	v_and_b32_e32 v115, 0xffff0000, v95
	v_lshlrev_b32_e32 v112, 16, v92
	v_and_b32_e32 v113, 0xffff0000, v92
	v_lshlrev_b32_e32 v118, 16, v93
	v_and_b32_e32 v119, 0xffff0000, v93
	v_lshlrev_b32_e32 v116, 16, v90
	v_and_b32_e32 v117, 0xffff0000, v90
	v_lshlrev_b32_e32 v122, 16, v91
	v_and_b32_e32 v123, 0xffff0000, v91
	v_lshlrev_b32_e32 v120, 16, v88
	v_and_b32_e32 v121, 0xffff0000, v88
	v_lshlrev_b32_e32 v126, 16, v89
	v_and_b32_e32 v127, 0xffff0000, v89
	v_lshlrev_b32_e32 v124, 16, v86
	v_and_b32_e32 v125, 0xffff0000, v86
	v_lshlrev_b32_e32 v130, 16, v87
	v_and_b32_e32 v131, 0xffff0000, v87
	v_lshlrev_b32_e32 v128, 16, v84
	v_and_b32_e32 v129, 0xffff0000, v84
	v_lshlrev_b32_e32 v134, 16, v85
	v_and_b32_e32 v135, 0xffff0000, v85
	s_waitcnt vmcnt(51)
	v_lshlrev_b32_e32 v82, 16, v80
	v_and_b32_e32 v83, 0xffff0000, v80
	v_lshlrev_b32_e32 v84, 16, v81
	v_and_b32_e32 v85, 0xffff0000, v81
	s_waitcnt vmcnt(50)
	v_lshlrev_b32_e32 v80, 16, v78
	v_and_b32_e32 v81, 0xffff0000, v78
	s_waitcnt vmcnt(33)
	v_cvt_pk_f32_fp8_e32 v[64:65], v146
	v_cvt_pk_f32_fp8_sdwa v[138:139], v146 src0_sel:WORD_1
	s_waitcnt vmcnt(32)
	v_cvt_pk_f32_fp8_sdwa v[144:145], v147 src0_sel:WORD_1
	v_pk_mul_f32 v[154:155], v[140:141], s[16:17] op_sel_hi:[1,0]
	v_cvt_pk_f32_fp8_e32 v[140:141], v147
	s_waitcnt vmcnt(31)
	v_cvt_pk_f32_fp8_e32 v[146:147], v148
	v_cvt_pk_f32_fp8_sdwa v[148:149], v148 src0_sel:WORD_1
	s_waitcnt vmcnt(30)
	v_cvt_pk_f32_fp8_e32 v[150:151], v152
	v_cvt_pk_f32_fp8_sdwa v[152:153], v152 src0_sel:WORD_1
	s_waitcnt vmcnt(26)
	v_cvt_pk_f32_fp8_e32 v[170:171], v168
	v_cvt_pk_f32_fp8_sdwa v[168:169], v168 src0_sel:WORD_1
	v_cvt_pk_f32_fp8_e32 v[160:161], v162
	v_mov_b32_e32 v179, v148
	v_mov_b32_e32 v181, v152
	v_cvt_pk_f32_fp8_e32 v[156:157], v158
	v_cvt_pk_f32_fp8_sdwa v[162:163], v162 src0_sel:WORD_1
	v_cvt_pk_f32_fp8_sdwa v[158:159], v158 src0_sel:WORD_1
	s_waitcnt vmcnt(24)
	v_cvt_pk_f32_fp8_sdwa v[210:211], v172 src0_sel:WORD_1
	s_waitcnt vmcnt(23)
	v_cvt_pk_f32_fp8_e32 v[208:209], v174
	s_waitcnt vmcnt(22)
	v_cvt_pk_f32_fp8_e32 v[214:215], v178
	s_waitcnt vmcnt(21)
	v_cvt_pk_f32_fp8_e32 v[218:219], v180
	v_cvt_pk_f32_fp8_sdwa v[212:213], v174 src0_sel:WORD_1
	v_cvt_pk_f32_fp8_sdwa v[216:217], v178 src0_sel:WORD_1
	v_cvt_pk_f32_fp8_sdwa v[220:221], v180 src0_sel:WORD_1
	v_mov_b32_e32 v178, v214
	v_mov_b32_e32 v148, v215
	s_waitcnt vmcnt(20)
	v_cvt_pk_f32_fp8_e32 v[214:215], v206
	v_mov_b32_e32 v180, v218
	v_mov_b32_e32 v152, v219
	s_waitcnt vmcnt(19)
	v_cvt_pk_f32_fp8_e32 v[218:219], v224
	v_cvt_pk_f32_fp8_sdwa v[222:223], v206 src0_sel:WORD_1
	v_cvt_pk_f32_fp8_sdwa v[224:225], v224 src0_sel:WORD_1
	v_pk_mul_f32 v[202:203], v[154:155], v[168:169]
	v_pk_mul_f32 v[204:205], v[154:155], v[168:169] op_sel_hi:[0,1]
	v_cvt_pk_f32_fp8_e32 v[168:169], v172
	v_cvt_pk_f32_fp8_e32 v[164:165], v166
	v_cvt_pk_f32_fp8_sdwa v[166:167], v166 src0_sel:WORD_1
	s_waitcnt vmcnt(18)
	v_cvt_pk_f32_fp8_e32 v[226:227], v228
	v_cvt_pk_f32_fp8_sdwa v[228:229], v228 src0_sel:WORD_1
	v_mov_b32_e32 v176, v140
	v_mov_b32_e32 v140, v144
	v_mov_b32_e32 v144, v146
	v_mov_b32_e32 v146, v150
	v_mov_b32_e32 v150, v160
	v_mov_b32_e32 v177, v208
	v_mov_b32_e32 v208, v141
	v_mov_b32_e32 v141, v212
	v_mov_b32_e32 v212, v145
	v_mov_b32_e32 v145, v216
	v_mov_b32_e32 v216, v147
	v_mov_b32_e32 v147, v220
	v_mov_b32_e32 v220, v151
	v_mov_b32_e32 v151, v218
	v_mov_b32_e32 v218, v161
	s_waitcnt vmcnt(17)
	v_cvt_pk_f32_fp8_e32 v[230:231], v232
	v_cvt_pk_f32_fp8_sdwa v[232:233], v232 src0_sel:WORD_1
	v_pk_mul_f32 v[210:211], v[154:155], v[210:211] op_sel:[1,0]
	v_pk_mul_f32 v[214:215], v[154:155], v[214:215] op_sel:[1,0]
	v_mov_b32_e32 v160, v162
	v_mov_b32_e32 v161, v224
	v_mov_b32_e32 v224, v163
	v_pk_mul_f32 v[222:223], v[154:155], v[222:223] op_sel:[1,0]
	v_pk_fma_f32 v[138:139], v[154:155], v[138:139], v[210:211] op_sel_hi:[0,1,1]
	v_pk_mul_f32 v[210:211], v[154:155], v[140:141]
	v_pk_mul_f32 v[144:145], v[154:155], v[144:145]
	v_pk_mul_f32 v[216:217], v[154:155], v[216:217]
	v_pk_fma_f32 v[140:141], v[154:155], v[156:157], v[214:215] op_sel_hi:[0,1,1]
	v_pk_mul_f32 v[150:151], v[154:155], v[150:151]
	v_pk_mul_f32 v[156:157], v[154:155], v[218:219]
	v_pk_mul_f32 v[234:235], v[154:155], v[168:169] op_sel:[1,0]
	s_waitcnt vmcnt(16)
	v_pk_mul_f32 v[168:169], v[142:143], s[16:17] op_sel_hi:[1,0]
	v_pk_mul_f32 v[220:221], v[154:155], v[220:221]
	v_pk_fma_f32 v[142:143], v[154:155], v[158:159], v[222:223] op_sel_hi:[0,1,1]
	v_pk_mul_f32 v[158:159], v[154:155], v[160:161]
	v_pk_mul_f32 v[160:161], v[154:155], v[224:225]
	v_pk_fma_f32 v[144:145], v[154:155], v[178:179], v[144:145] op_sel:[1,0,0] op_sel_hi:[0,1,1]
	v_pk_fma_f32 v[178:179], v[154:155], v[148:149], v[216:217] op_sel:[1,0,0] op_sel_hi:[0,1,1]
	v_mov_b32_e32 v148, v150
	v_mov_b32_e32 v149, v156
	v_mov_b32_e32 v156, v151
	v_mov_b32_e32 v162, v164
	v_mov_b32_e32 v164, v166
	v_mov_b32_e32 v163, v226
	v_mov_b32_e32 v226, v165
	v_mov_b32_e32 v165, v228
	v_mov_b32_e32 v228, v167
	v_pk_mul_f32 v[146:147], v[154:155], v[146:147]
	v_pk_fma_f32 v[220:221], v[154:155], v[152:153], v[220:221] op_sel:[1,0,0] op_sel_hi:[0,1,1]
	v_pk_add_f32 v[148:149], v[148:149], v[156:157]
	v_mov_b32_e32 v152, v158
	v_mov_b32_e32 v153, v160
	v_mov_b32_e32 v160, v159
	v_mov_b32_e32 v173, v154
	v_mov_b32_e32 v175, v154
	v_pk_mul_f32 v[200:201], v[154:155], v[170:171]
	v_pk_mul_f32 v[236:237], v[154:155], v[230:231] op_sel_hi:[1,0]
	v_pk_mul_f32 v[166:167], v[154:155], v[232:233] op_sel_hi:[1,0]
	v_pk_mul_f32 v[232:233], v[154:155], v[232:233]
	v_pk_fma_f32 v[64:65], v[154:155], v[64:65], v[234:235] op_sel_hi:[0,1,1]
	v_pk_mul_f32 v[176:177], v[154:155], v[176:177]
	v_pk_mul_f32 v[208:209], v[154:155], v[208:209]
	v_pk_mul_f32 v[212:213], v[154:155], v[212:213]
	v_pk_mul_f32 v[162:163], v[154:155], v[162:163]
	v_pk_mul_f32 v[214:215], v[154:155], v[226:227]
	v_pk_mul_f32 v[164:165], v[154:155], v[164:165]
	v_pk_mul_f32 v[218:219], v[154:155], v[228:229]
	v_pk_fma_f32 v[146:147], v[154:155], v[180:181], v[146:147] op_sel:[1,0,0] op_sel_hi:[0,1,1]
	v_mov_b32_e32 v154, v149
	v_mov_b32_e32 v230, v149
	v_pk_add_f32 v[152:153], v[152:153], v[160:161]
	v_pk_mul_f32 v[150:151], v[154:155], v[230:231]
	v_mov_b32_e32 v154, v153
	v_mov_b32_e32 v230, v153
	v_mov_b32_e32 v203, v171
	v_mov_b32_e32 v207, v202
	v_pk_mul_f32 v[154:155], v[154:155], v[230:231]
	v_mov_b32_e32 v174, v152
	v_mov_b32_e32 v202, v152
	v_mov_b32_e32 v156, v176
	v_mov_b32_e32 v157, v208
	v_mov_b32_e32 v208, v177
	v_pk_fma_f32 v[174:175], v[174:175], v[202:203], v[154:155]
	v_mov_b32_e32 v154, v162
	v_mov_b32_e32 v155, v214
	v_mov_b32_e32 v214, v163
	v_mov_b32_e32 v162, v164
	v_mov_b32_e32 v163, v218
	v_mov_b32_e32 v218, v165
	v_pk_mul_f32 v[164:165], v[178:179], v[178:179]
	v_mov_b32_e32 v176, v210
	v_mov_b32_e32 v177, v212
	v_mov_b32_e32 v212, v211
	v_pk_add_f32 v[158:159], v[156:157], v[208:209]
	v_mul_f32_e32 v166, v141, v141
	v_pk_add_f32 v[156:157], v[162:163], v[218:219]
	v_mov_b32_e32 v162, v145
	v_pk_fma_f32 v[208:209], v[144:145], v[144:145], v[164:165]
	v_mov_b32_e32 v145, v178
	v_mul_f32_e32 v178, v143, v143
	v_pk_add_f32 v[160:161], v[176:177], v[212:213]
	v_mov_b32_e32 v163, v179
	v_pk_fma_f32 v[212:213], v[140:141], v[140:141], v[166:167] op_sel_hi:[1,1,0]
	v_pk_fma_f32 v[178:179], v[142:143], v[142:143], v[178:179] op_sel_hi:[1,1,0]
	v_pk_mul_f32 v[176:177], v[220:221], v[220:221]
	v_mov_b32_e32 v213, v200
	v_mov_b32_e32 v179, v237
	v_pk_fma_f32 v[176:177], v[146:147], v[146:147], v[176:177]
	v_pk_add_f32 v[178:179], v[212:213], v[178:179]
	v_mov_b32_e32 v212, v139
	v_mov_b32_e32 v213, v161
	v_mov_b32_e32 v172, v148
	v_mov_b32_e32 v170, v148
	v_mov_b32_e32 v202, v65
	v_mov_b32_e32 v246, v138
	v_pk_add_f32 v[154:155], v[154:155], v[214:215]
	v_mov_b32_e32 v203, v159
	v_mov_b32_e32 v247, v160
	v_pk_mul_f32 v[212:213], v[212:213], v[212:213]
	v_pk_add_f32 v[176:177], v[176:177], v[176:177] op_sel:[0,1] op_sel_hi:[1,0]
	s_waitcnt vmcnt(12)
	v_cvt_pk_f32_fp8_e32 v[216:217], v241
	v_pk_fma_f32 v[150:151], v[172:173], v[170:171], v[150:151]
	s_waitcnt vmcnt(10)
	v_cvt_pk_f32_fp8_e32 v[170:171], v244
	v_mov_b32_e32 v230, v64
	v_mov_b32_e32 v231, v158
	v_mov_b32_e32 v206, v154
	v_mov_b32_e32 v166, v154
	v_mov_b32_e32 v204, v156
	v_mov_b32_e32 v232, v156
	v_pk_mul_f32 v[202:203], v[202:203], v[202:203]
	v_pk_fma_f32 v[212:213], v[246:247], v[246:247], v[212:213]
	v_mov_b32_e32 v177, v237
	s_waitcnt vmcnt(4)
	v_cvt_pk_f32_fp8_sdwa v[236:237], v250 src0_sel:WORD_1
	s_waitcnt vmcnt(2)
	v_cvt_pk_f32_fp8_e32 v[246:247], v251
	v_cvt_pk_f32_fp8_sdwa v[228:229], v239 src0_sel:WORD_1
	v_pk_add_f32 v[206:207], v[206:207], v[166:167]
	v_mul_f32_e32 v214, v155, v155
	v_pk_add_f32 v[166:167], v[204:205], v[232:233]
	v_mul_f32_e32 v204, v157, v157
	v_pk_fma_f32 v[202:203], v[230:231], v[230:231], v[202:203]
	v_cvt_pk_f32_fp8_sdwa v[232:233], v248 src0_sel:WORD_1
	v_pk_fma_f32 v[214:215], v[154:155], v[154:155], v[214:215] op_sel_hi:[1,1,0]
	v_pk_fma_f32 v[204:205], v[156:157], v[156:157], v[204:205] op_sel_hi:[1,1,0]
	v_pk_add_f32 v[202:203], v[202:203], v[212:213]
	v_pk_mul_f32 v[212:213], v[166:167], v[166:167]
	v_mov_b32_e32 v166, v207
	v_pk_mul_f32 v[206:207], v[206:207], v[206:207]
	v_pk_add_f32 v[208:209], v[208:209], v[208:209] op_sel:[0,1] op_sel_hi:[1,0]
	v_mov_b32_e32 v215, v207
	v_mov_b32_e32 v205, v213
	v_pk_add_f32 v[202:203], v[202:203], v[202:203] op_sel:[0,1] op_sel_hi:[1,0]
	v_pk_add_f32 v[204:205], v[214:215], v[204:205]
	v_mov_b32_e32 v214, v216
	v_pk_add_f32 v[202:203], v[202:203], v[208:209]
	v_pk_add_f32 v[208:209], v[150:151], v[174:175]
	v_pk_mul_f32 v[174:175], v[150:151], v[174:175]
	v_mov_b32_e32 v216, v170
	v_mov_b32_e32 v215, v236
	v_mov_b32_e32 v236, v217
	v_mov_b32_e32 v217, v246
	v_mov_b32_e32 v246, v171
	v_cvt_pk_f32_fp8_e32 v[170:171], v186
	v_cvt_pk_f32_fp8_e32 v[222:223], v238
	v_cvt_pk_f32_fp8_e32 v[226:227], v239
	v_cvt_pk_f32_fp8_sdwa v[172:173], v244 src0_sel:WORD_1
	v_mov_b32_e32 v164, v147
	v_mov_b32_e32 v165, v221
	v_mov_b32_e32 v147, v220
	v_mov_b32_e32 v220, v228
	v_mov_b32_e32 v209, v175
	v_cvt_pk_f32_fp8_e32 v[230:231], v248
	v_mov_b32_e32 v221, v232
	v_mov_b32_e32 v232, v229
	v_cvt_pk_f32_fp8_e32 v[174:175], v249
	v_cvt_pk_f32_fp8_sdwa v[228:229], v249 src0_sel:WORD_1
	v_cvt_pk_f32_fp8_sdwa v[248:249], v251 src0_sel:WORD_1
	v_cvt_pk_f32_fp8_sdwa v[224:225], v238 src0_sel:WORD_1
	v_cvt_pk_f32_fp8_sdwa v[238:239], v240 src0_sel:WORD_1
	v_pk_mul_f32 v[170:171], v[168:169], v[170:171] op_sel:[1,0]
	v_mov_b32_e32 v218, v226
	v_mov_b32_e32 v219, v230
	v_mov_b32_e32 v230, v227
	v_mov_b32_e32 v226, v172
	v_mov_b32_e32 v227, v248
	v_mov_b32_e32 v248, v173
	v_pk_fma_f32 v[172:173], v[168:169], v[222:223], v[170:171] op_sel_hi:[0,1,1]
	v_cvt_pk_f32_fp8_sdwa v[170:171], v186 src0_sel:WORD_1
	v_cvt_pk_f32_fp8_e32 v[234:235], v240
	v_cvt_pk_f32_fp8_sdwa v[240:241], v241 src0_sel:WORD_1
	v_mov_b32_e32 v201, v238
	v_mov_b32_e32 v203, v200
	v_mov_b32_e32 v200, v174
	v_mov_b32_e32 v238, v175
	v_cvt_pk_f32_fp8_e32 v[174:175], v250
	v_pk_mul_f32 v[170:171], v[168:169], v[170:171] op_sel:[1,0]
	v_mov_b32_e32 v213, v240
	v_cvt_pk_f32_fp8_e32 v[180:181], v242
	v_mov_b32_e32 v212, v174
	v_mov_b32_e32 v240, v175
	v_pk_fma_f32 v[174:175], v[168:169], v[224:225], v[170:171] op_sel_hi:[0,1,1]
	v_cvt_pk_f32_fp8_e32 v[170:171], v187
	v_cvt_pk_f32_fp8_e32 v[210:211], v245
	s_waitcnt vmcnt(1)
	v_cvt_pk_f32_fp8_e32 v[250:251], v252
	v_cvt_pk_f32_fp8_sdwa v[244:245], v245 src0_sel:WORD_1
	v_cvt_pk_f32_fp8_sdwa v[252:253], v252 src0_sel:WORD_1
	v_cvt_pk_f32_fp8_sdwa v[222:223], v254 src0_sel:WORD_1
	v_pk_mul_f32 v[170:171], v[168:169], v[170:171] op_sel:[1,0]
	v_mov_b32_e32 v207, v228
	v_mov_b32_e32 v228, v235
	v_pk_add_f32 v[202:203], v[202:203], v[176:177]
	v_pk_fma_f32 v[170:171], v[168:169], v[180:181], v[170:171] op_sel_hi:[0,1,1]
	v_pk_mul_f32 v[180:181], v[168:169], v[218:219]
	v_pk_mul_f32 v[218:219], v[168:169], v[230:231]
	v_mov_b32_e32 v206, v234
	v_cvt_pk_f32_fp8_sdwa v[176:177], v187 src0_sel:WORD_1
	v_pk_mul_f32 v[224:225], v[168:169], v[232:233]
	v_pk_add_f32 v[230:231], v[202:203], v[178:179]
	v_pk_mul_f32 v[232:233], v[202:203], v[178:179]
	v_mov_b32_e32 v150, v203
	v_mov_b32_e32 v202, v180
	v_mov_b32_e32 v203, v218
	v_mov_b32_e32 v218, v181
	v_pk_mul_f32 v[180:181], v[168:169], v[228:229]
	v_cvt_pk_f32_fp8_sdwa v[242:243], v242 src0_sel:WORD_1
	v_mov_b32_e32 v235, v250
	v_mov_b32_e32 v250, v211
	v_pk_mul_f32 v[178:179], v[168:169], v[206:207]
	v_pk_fma_f32 v[206:207], v[168:169], v[238:239], v[180:181] op_sel:[1,0,0] op_sel_hi:[0,1,1]
	v_pk_mul_f32 v[180:181], v[168:169], v[214:215]
	v_mov_b32_e32 v234, v210
	v_mov_b32_e32 v210, v244
	v_mov_b32_e32 v211, v252
	v_mov_b32_e32 v252, v245
	v_cvt_pk_f32_fp8_e32 v[244:245], v254
	v_pk_fma_f32 v[180:181], v[168:169], v[212:213], v[180:181] op_sel:[1,0,0] op_sel_hi:[0,1,1]
	v_pk_mul_f32 v[212:213], v[168:169], v[222:223]
	v_pk_mul_f32 v[214:215], v[168:169], v[222:223] op_sel_hi:[0,1]
	v_pk_mul_f32 v[222:223], v[168:169], v[236:237]
	v_pk_mul_f32 v[236:237], v[168:169], v[246:247]
	v_pk_mul_f32 v[246:247], v[168:169], v[250:251]
	v_mov_b32_e32 v231, v233
	s_waitcnt vmcnt(0)
	v_cvt_pk_f32_fp8_e32 v[232:233], v188
	v_cvt_pk_f32_fp8_sdwa v[250:251], v188 src0_sel:WORD_1
	v_pk_mul_f32 v[176:177], v[168:169], v[176:177] op_sel:[1,0]
	v_pk_mul_f32 v[220:221], v[168:169], v[220:221]
	v_pk_mul_f32 v[216:217], v[168:169], v[216:217]
	v_pk_mul_f32 v[226:227], v[168:169], v[226:227]
	v_pk_mul_f32 v[238:239], v[168:169], v[248:249]
	v_pk_mul_f32 v[234:235], v[168:169], v[234:235]
	v_pk_mul_f32 v[210:211], v[168:169], v[210:211]
	v_pk_mul_f32 v[248:249], v[168:169], v[252:253]
	v_pk_fma_f32 v[176:177], v[168:169], v[242:243], v[176:177] op_sel_hi:[0,1,1]
	v_mov_b32_e32 v242, v220
	v_mov_b32_e32 v243, v224
	v_mov_b32_e32 v224, v221
	v_pk_fma_f32 v[222:223], v[168:169], v[240:241], v[222:223] op_sel:[1,0,0] op_sel_hi:[0,1,1]
	v_mov_b32_e32 v240, v216
	v_mov_b32_e32 v241, v236
	v_mov_b32_e32 v236, v217
	v_mov_b32_e32 v216, v226
	v_mov_b32_e32 v217, v238
	v_mov_b32_e32 v238, v227
	v_mov_b32_e32 v226, v234
	v_mov_b32_e32 v227, v246
	v_mov_b32_e32 v246, v235
	v_mov_b32_e32 v234, v210
	v_mov_b32_e32 v235, v248
	v_mov_b32_e32 v248, v211
	v_mov_b32_e32 v221, v168
	v_pk_fma_f32 v[178:179], v[168:169], v[200:201], v[178:179] op_sel:[1,0,0] op_sel_hi:[0,1,1]
	v_mov_b32_e32 v201, v168
	v_pk_mul_f32 v[228:229], v[168:169], v[244:245]
	v_pk_add_f32 v[202:203], v[202:203], v[218:219]
	v_pk_mul_f32 v[218:219], v[168:169], v[232:233] op_sel_hi:[1,0]
	v_pk_add_f32 v[224:225], v[242:243], v[224:225]
	v_pk_mul_f32 v[242:243], v[168:169], v[250:251] op_sel_hi:[1,0]
	v_pk_mul_f32 v[250:251], v[168:169], v[250:251]
	v_pk_add_f32 v[226:227], v[226:227], v[246:247]
	v_pk_mul_f32 v[246:247], v[206:207], v[206:207]
	v_pk_add_f32 v[234:235], v[234:235], v[248:249]
	v_pk_mul_f32 v[248:249], v[222:223], v[222:223]
	v_pk_add_f32 v[208:209], v[230:231], v[208:209]
	v_mul_f32_e32 v168, v171, v171
	v_mul_f32_e32 v200, v177, v177
	v_mov_b32_e32 v213, v212
	v_mov_b32_e32 v230, v179
	v_mov_b32_e32 v231, v207
	v_pk_fma_f32 v[246:247], v[178:179], v[178:179], v[246:247]
	v_mov_b32_e32 v179, v206
	v_mov_b32_e32 v206, v181
	v_mov_b32_e32 v207, v223
	v_pk_fma_f32 v[248:249], v[180:181], v[180:181], v[248:249]
	v_mov_b32_e32 v181, v222
	v_pk_add_f32 v[204:205], v[208:209], v[204:205]
	v_pk_fma_f32 v[208:209], v[170:171], v[170:171], v[168:169] op_sel_hi:[1,1,0]
	v_pk_fma_f32 v[222:223], v[176:177], v[176:177], v[200:201] op_sel_hi:[1,1,0]
	v_mov_b32_e32 v212, v226
	v_mov_b32_e32 v242, v226
	v_pk_add_f32 v[236:237], v[240:241], v[236:237]
	v_pk_add_f32 v[216:217], v[216:217], v[238:239]
	v_mov_b32_e32 v238, v173
	v_mov_b32_e32 v209, v228
	v_mov_b32_e32 v223, v219
	v_pk_add_f32 v[212:213], v[212:213], v[242:243]
	v_mov_b32_e32 v242, v175
	v_mov_b32_e32 v239, v203
	v_mov_b32_e32 v243, v225
	v_mov_b32_e32 v240, v172
	v_pk_add_f32 v[208:209], v[208:209], v[222:223]
	v_mov_b32_e32 v222, v174
	v_mov_b32_e32 v241, v202
	v_mov_b32_e32 v223, v224
	v_mov_b32_e32 v168, v237
	v_mov_b32_e32 v232, v237
	v_mov_b32_e32 v214, v234
	v_mov_b32_e32 v250, v234
	v_pk_mul_f32 v[238:239], v[238:239], v[238:239]
	v_pk_mul_f32 v[242:243], v[242:243], v[242:243]
	v_add_f32_e32 v186, v204, v205
	v_mov_b32_e32 v220, v236
	v_mov_b32_e32 v244, v236
	v_pk_add_f32 v[214:215], v[214:215], v[250:251]
	v_mul_f32_e32 v218, v227, v227
	v_pk_fma_f32 v[238:239], v[240:241], v[240:241], v[238:239]
	v_pk_add_f32 v[248:249], v[248:249], v[248:249] op_sel:[0,1] op_sel_hi:[1,0]
	v_pk_fma_f32 v[222:223], v[222:223], v[222:223], v[242:243]
	v_pk_mul_f32 v[242:243], v[168:169], v[232:233]
	v_mov_b32_e32 v168, v217
	v_mov_b32_e32 v232, v217
	ds_bpermute_b32 v187, v199, v186
	v_mov_b32_e32 v211, v245
	v_mov_b32_e32 v200, v216
	v_mov_b32_e32 v210, v216
	v_pk_fma_f32 v[250:251], v[226:227], v[226:227], v[218:219] op_sel_hi:[1,1,0]
	v_mov_b32_e32 v249, v219
	v_pk_mul_f32 v[168:169], v[168:169], v[232:233]
	v_pk_fma_f32 v[204:205], v[220:221], v[244:245], v[242:243]
	v_pk_mul_f32 v[218:219], v[212:213], v[212:213]
	v_pk_mul_f32 v[220:221], v[214:215], v[214:215]
	v_mov_b32_e32 v214, v213
	v_pk_add_f32 v[212:213], v[238:239], v[222:223]
	v_pk_add_f32 v[246:247], v[246:247], v[246:247] op_sel:[0,1] op_sel_hi:[1,0]
	v_pk_fma_f32 v[168:169], v[200:201], v[210:211], v[168:169]
	v_pk_add_f32 v[200:201], v[212:213], v[212:213] op_sel:[0,1] op_sel_hi:[1,0]
	v_pk_add_f32 v[210:211], v[204:205], v[168:169]
	v_pk_add_f32 v[200:201], v[200:201], v[246:247]
	v_pk_mul_f32 v[168:169], v[204:205], v[168:169]
	v_mov_b32_e32 v201, v228
	v_mul_f32_e32 v240, v235, v235
	v_mov_b32_e32 v211, v169
	v_pk_add_f32 v[168:169], v[200:201], v[248:249]
	s_waitcnt lgkmcnt(0)
	v_add_f32_e32 v186, v186, v187
	v_pk_fma_f32 v[240:241], v[234:235], v[234:235], v[240:241] op_sel_hi:[1,1,0]
	v_pk_add_f32 v[200:201], v[168:169], v[208:209]
	v_pk_mul_f32 v[208:209], v[168:169], v[208:209]
	ds_bpermute_b32 v187, v198, v186
	v_mov_b32_e32 v251, v219
	v_mov_b32_e32 v241, v221
	v_mov_b32_e32 v201, v209
	v_pk_add_f32 v[212:213], v[250:251], v[240:241]
	v_mov_b32_e32 v204, v169
	v_pk_add_f32 v[168:169], v[200:201], v[210:211]
	s_waitcnt lgkmcnt(0)
	v_add_f32_e32 v186, v186, v187
	v_pk_add_f32 v[168:169], v[168:169], v[212:213]
	ds_bpermute_b32 v187, v197, v186
	v_add_f32_e32 v168, v168, v169
	ds_bpermute_b32 v169, v199, v168
	v_lshlrev_b32_e32 v86, 16, v79
	v_and_b32_e32 v87, 0xffff0000, v79
	s_waitcnt lgkmcnt(1)
	v_add_f32_e32 v186, v186, v187
	ds_bpermute_b32 v187, v196, v186
	s_waitcnt lgkmcnt(1)
	v_add_f32_e32 v168, v168, v169
	ds_bpermute_b32 v169, v198, v168
	v_lshlrev_b32_e32 v78, 16, v76
	v_and_b32_e32 v79, 0xffff0000, v76
	s_waitcnt lgkmcnt(1)
	v_add_f32_e32 v186, v186, v187
	ds_bpermute_b32 v187, v195, v186
	s_waitcnt lgkmcnt(1)
	v_add_f32_e32 v168, v168, v169
	ds_bpermute_b32 v169, v197, v168
	v_lshlrev_b32_e32 v88, 16, v77
	v_and_b32_e32 v89, 0xffff0000, v77
	s_waitcnt lgkmcnt(1)
	v_add_f32_e32 v186, v186, v187
	ds_bpermute_b32 v187, v194, v186
	s_waitcnt lgkmcnt(1)
	v_add_f32_e32 v168, v168, v169
	ds_bpermute_b32 v169, v196, v168
	v_lshlrev_b32_e32 v76, 16, v74
	v_and_b32_e32 v77, 0xffff0000, v74
	s_waitcnt lgkmcnt(1)
	v_add_f32_e32 v186, v186, v187
	v_fmamk_f32 v186, v186, 0x3a000000, v192
	s_waitcnt lgkmcnt(0)
	v_add_f32_e32 v168, v168, v169
	ds_bpermute_b32 v169, v195, v168
	v_mul_f32_e32 v187, 0x4f800000, v186
	v_cmp_gt_f32_e32 vcc, s30, v186
	v_lshlrev_b32_e32 v90, 16, v75
	v_and_b32_e32 v91, 0xffff0000, v75
	v_cndmask_b32_e32 v186, v186, v187, vcc
	v_sqrt_f32_e32 v187, v186
	s_waitcnt lgkmcnt(0)
	v_add_f32_e32 v168, v168, v169
	ds_bpermute_b32 v169, v194, v168
	v_lshlrev_b32_e32 v74, 16, v72
	v_add_u32_e32 v188, -1, v187
	v_add_u32_e32 v194, 1, v187
	v_fma_f32 v195, -v188, v187, v186
	v_fma_f32 v196, -v194, v187, v186
	v_cmp_ge_f32_e64 s[0:1], 0, v195
	s_waitcnt lgkmcnt(0)
	v_add_f32_e32 v168, v168, v169
	v_fmamk_f32 v168, v168, 0x3a000000, v192
	v_cndmask_b32_e64 v187, v187, v188, s[0:1]
	v_cmp_lt_f32_e64 s[0:1], 0, v196
	v_mul_f32_e32 v188, 0x4f800000, v168
	v_and_b32_e32 v75, 0xffff0000, v72
	v_cndmask_b32_e64 v169, v187, v194, s[0:1]
	v_mul_f32_e32 v187, 0x37800000, v169
	v_cmp_gt_f32_e64 s[0:1], s30, v168
	v_cndmask_b32_e32 v169, v169, v187, vcc
	v_cmp_class_f32_e32 vcc, v186, v193
	v_cndmask_b32_e64 v168, v168, v188, s[0:1]
	v_lshlrev_b32_e32 v92, 16, v73
	v_cndmask_b32_e32 v169, v169, v186, vcc
	v_sqrt_f32_e32 v186, v168
	v_div_scale_f32 v187, s[2:3], v169, v169, 1.0
	v_rcp_f32_e32 v194, v187
	v_add_u32_e32 v195, -1, v186
	v_add_u32_e32 v196, 1, v186
	v_fma_f32 v197, -v195, v186, v168
	v_fma_f32 v198, -v196, v186, v168
	v_cmp_ge_f32_e64 s[2:3], 0, v197
	v_fma_f32 v199, -v187, v194, 1.0
	v_div_scale_f32 v188, vcc, 1.0, v169, 1.0
	v_cndmask_b32_e64 v186, v186, v195, s[2:3]
	v_cmp_lt_f32_e64 s[2:3], 0, v198
	v_fmac_f32_e32 v194, v199, v194
	v_mul_f32_e32 v195, v188, v194
	v_cndmask_b32_e64 v186, v186, v196, s[2:3]
	v_mul_f32_e32 v196, 0x37800000, v186
	v_fma_f32 v197, -v187, v195, v188
	v_cndmask_b32_e64 v186, v186, v196, s[0:1]
	v_cmp_class_f32_e64 s[0:1], v168, v193
	v_fmac_f32_e32 v195, v197, v194
	v_and_b32_e32 v93, 0xffff0000, v73
	v_cndmask_b32_e64 v186, v186, v168, s[0:1]
	v_fma_f32 v168, -v187, v195, v188
	v_div_scale_f32 v187, s[0:1], v186, v186, 1.0
	v_div_fmas_f32 v168, v168, v194, v195
	v_rcp_f32_e32 v194, v187
	v_div_fixup_f32 v168, v168, v169, 1.0
	v_pk_mul_f32 v[138:139], v[138:139], v[168:169] op_sel_hi:[1,0]
	v_pk_mul_f32 v[64:65], v[64:65], v[168:169] op_sel_hi:[1,0]
	v_pk_mul_f32 v[140:141], v[140:141], v[168:169] op_sel_hi:[1,0]
	v_pk_mul_f32 v[64:65], v[28:29], v[64:65]
	v_pk_mul_f32 v[138:139], v[30:31], v[138:139]
	v_pk_mul_f32 v[160:161], v[160:161], v[168:169] op_sel_hi:[1,0]
	v_pk_mul_f32 v[158:159], v[158:159], v[168:169] op_sel_hi:[1,0]
	v_pk_mul_f32 v[162:163], v[162:163], v[168:169] op_sel_hi:[1,0]
	v_pk_mul_f32 v[144:145], v[144:145], v[168:169] op_sel_hi:[1,0]
	v_pk_mul_f32 v[164:165], v[164:165], v[168:169] op_sel_hi:[1,0]
	v_pk_mul_f32 v[146:147], v[146:147], v[168:169] op_sel_hi:[1,0]
	v_pk_mul_f32 v[142:143], v[142:143], v[168:169] op_sel_hi:[1,0]
	v_pk_mul_f32 v[152:153], v[152:153], v[168:169] op_sel_hi:[1,0]
	v_pk_mul_f32 v[148:149], v[148:149], v[168:169] op_sel_hi:[1,0]
	v_pk_mul_f32 v[156:157], v[156:157], v[168:169] op_sel_hi:[1,0]
	v_pk_mul_f32 v[154:155], v[154:155], v[168:169] op_sel_hi:[1,0]
	v_pk_mul_f32 v[166:167], v[166:167], v[168:169] op_sel_hi:[1,0]
	v_pk_mul_f32 v[150:151], v[150:151], v[168:169] op_sel_hi:[1,0]
	v_pk_mul_f32 v[168:169], v[24:25], v[140:141]
	v_pk_fma_f32 v[140:141], v[46:47], v[138:139], v[110:111]
	v_pk_fma_f32 v[138:139], v[44:45], v[64:65], v[106:107]
	v_fma_f32 v64, -v187, v194, 1.0
	v_div_scale_f32 v188, s[0:1], 1.0, v186, 1.0
	v_fmac_f32_e32 v194, v64, v194
	v_mul_f32_e32 v64, v188, v194
	v_fma_f32 v65, -v187, v64, v188
	v_fmac_f32_e32 v64, v65, v194
	v_fma_f32 v65, -v187, v64, v188
	s_mov_b64 vcc, s[0:1]
	v_div_fmas_f32 v64, v65, v194, v64
	v_pk_mul_f32 v[158:159], v[20:21], v[158:159]
	v_pk_mul_f32 v[160:161], v[22:23], v[160:161]
	v_pk_mul_f32 v[144:145], v[12:13], v[144:145]
	v_pk_mul_f32 v[162:163], v[14:15], v[162:163]
	v_pk_mul_f32 v[146:147], v[4:5], v[146:147]
	v_pk_mul_f32 v[164:165], v[6:7], v[164:165]
	v_pk_mul_f32 v[142:143], v[26:27], v[142:143]
	v_pk_mul_f32 v[148:149], v[16:17], v[148:149]
	v_pk_mul_f32 v[152:153], v[18:19], v[152:153]
	v_pk_mul_f32 v[154:155], v[8:9], v[154:155]
	v_pk_mul_f32 v[156:157], v[10:11], v[156:157]
	v_pk_mul_f32 v[150:151], v[0:1], v[150:151]
	v_pk_mul_f32 v[166:167], v[2:3], v[166:167]
	v_div_fixup_f32 v64, v64, v186, 1.0
	v_pk_fma_f32 v[110:111], v[42:43], v[160:161], v[114:115]
	v_pk_fma_f32 v[108:109], v[40:41], v[158:159], v[108:109]
	v_pk_fma_f32 v[114:115], v[38:39], v[162:163], v[118:119]
	v_pk_fma_f32 v[112:113], v[36:37], v[144:145], v[112:113]
	v_pk_fma_f32 v[118:119], v[34:35], v[164:165], v[122:123]
	v_pk_fma_f32 v[116:117], v[32:33], v[146:147], v[116:117]
	v_pk_fma_f32 v[122:123], v[62:63], v[142:143], v[126:127]
	v_pk_fma_f32 v[120:121], v[60:61], v[168:169], v[120:121]
	v_pk_fma_f32 v[126:127], v[58:59], v[152:153], v[130:131]
	v_pk_fma_f32 v[124:125], v[56:57], v[148:149], v[124:125]
	v_pk_fma_f32 v[130:131], v[54:55], v[156:157], v[134:135]
	v_pk_fma_f32 v[128:129], v[52:53], v[154:155], v[128:129]
	v_pk_fma_f32 v[134:135], v[50:51], v[166:167], v[136:137]
	v_pk_fma_f32 v[132:133], v[48:49], v[150:151], v[132:133]
	global_store_dwordx4 v[100:101], v[138:141], off
	global_store_dwordx4 v[100:101], v[108:111], off offset:1024
	global_store_dwordx4 v[100:101], v[112:115], off offset:2048
	global_store_dwordx4 v[100:101], v[116:119], off offset:3072
	global_store_dwordx4 v[102:103], v[120:123], off
	global_store_dwordx4 v[102:103], v[124:127], off offset:1024
	global_store_dwordx4 v[102:103], v[128:131], off offset:2048
	global_store_dwordx4 v[102:103], v[132:135], off offset:3072
	v_pk_mul_f32 v[100:101], v[174:175], v[64:65] op_sel_hi:[1,0]
	v_pk_mul_f32 v[102:103], v[172:173], v[64:65] op_sel_hi:[1,0]
	v_pk_mul_f32 v[106:107], v[224:225], v[64:65] op_sel_hi:[1,0]
	v_pk_mul_f32 v[108:109], v[202:203], v[64:65] op_sel_hi:[1,0]
	v_pk_mul_f32 v[110:111], v[230:231], v[64:65] op_sel_hi:[1,0]
	v_pk_mul_f32 v[112:113], v[178:179], v[64:65] op_sel_hi:[1,0]
	v_pk_mul_f32 v[114:115], v[206:207], v[64:65] op_sel_hi:[1,0]
	v_pk_mul_f32 v[116:117], v[180:181], v[64:65] op_sel_hi:[1,0]
	v_pk_mul_f32 v[118:119], v[176:177], v[64:65] op_sel_hi:[1,0]
	v_pk_mul_f32 v[120:121], v[170:171], v[64:65] op_sel_hi:[1,0]
	v_pk_mul_f32 v[122:123], v[216:217], v[64:65] op_sel_hi:[1,0]
	v_pk_mul_f32 v[124:125], v[236:237], v[64:65] op_sel_hi:[1,0]
	v_pk_mul_f32 v[126:127], v[234:235], v[64:65] op_sel_hi:[1,0]
	v_pk_mul_f32 v[128:129], v[226:227], v[64:65] op_sel_hi:[1,0]
	v_pk_mul_f32 v[130:131], v[214:215], v[64:65] op_sel_hi:[1,0]
	v_pk_mul_f32 v[64:65], v[204:205], v[64:65] op_sel_hi:[1,0]
	v_pk_mul_f32 v[28:29], v[28:29], v[102:103]
	v_pk_mul_f32 v[30:31], v[30:31], v[100:101]
	v_lshlrev_b32_e32 v72, 16, v70
	v_and_b32_e32 v73, 0xffff0000, v70
	v_lshlrev_b32_e32 v94, 16, v71
	v_and_b32_e32 v95, 0xffff0000, v71
	v_lshlrev_b32_e32 v70, 16, v68
	v_and_b32_e32 v71, 0xffff0000, v68
	v_lshlrev_b32_e32 v96, 16, v69
	v_and_b32_e32 v97, 0xffff0000, v69
	v_lshlrev_b32_e32 v68, 16, v66
	v_and_b32_e32 v69, 0xffff0000, v66
	v_lshlrev_b32_e32 v66, 16, v67
	v_and_b32_e32 v67, 0xffff0000, v67
	v_pk_mul_f32 v[20:21], v[20:21], v[108:109]
	v_pk_mul_f32 v[22:23], v[22:23], v[106:107]
	v_pk_mul_f32 v[12:13], v[12:13], v[112:113]
	v_pk_mul_f32 v[14:15], v[14:15], v[110:111]
	v_pk_mul_f32 v[100:101], v[4:5], v[116:117]
	v_pk_mul_f32 v[102:103], v[6:7], v[114:115]
	v_pk_mul_f32 v[24:25], v[24:25], v[120:121]
	v_pk_mul_f32 v[26:27], v[26:27], v[118:119]
	v_pk_mul_f32 v[106:107], v[16:17], v[124:125]
	v_pk_mul_f32 v[108:109], v[18:19], v[122:123]
	v_pk_mul_f32 v[110:111], v[8:9], v[128:129]
	v_pk_mul_f32 v[112:113], v[10:11], v[126:127]
	v_pk_mul_f32 v[64:65], v[0:1], v[64:65]
	v_pk_mul_f32 v[114:115], v[2:3], v[130:131]
	v_pk_fma_f32 v[2:3], v[46:47], v[30:31], v[84:85]
	v_pk_fma_f32 v[0:1], v[44:45], v[28:29], v[82:83]
	v_pk_fma_f32 v[6:7], v[42:43], v[22:23], v[86:87]
	v_pk_fma_f32 v[4:5], v[40:41], v[20:21], v[80:81]
	v_pk_fma_f32 v[10:11], v[38:39], v[14:15], v[88:89]
	v_pk_fma_f32 v[8:9], v[36:37], v[12:13], v[78:79]
	v_pk_fma_f32 v[14:15], v[34:35], v[102:103], v[90:91]
	v_pk_fma_f32 v[12:13], v[32:33], v[100:101], v[76:77]
	v_pk_fma_f32 v[18:19], v[62:63], v[26:27], v[92:93]
	v_pk_fma_f32 v[16:17], v[60:61], v[24:25], v[74:75]
	v_pk_fma_f32 v[22:23], v[58:59], v[108:109], v[94:95]
	v_pk_fma_f32 v[20:21], v[56:57], v[106:107], v[72:73]
	v_pk_fma_f32 v[26:27], v[54:55], v[112:113], v[96:97]
	v_pk_fma_f32 v[24:25], v[52:53], v[110:111], v[70:71]
	v_pk_fma_f32 v[30:31], v[50:51], v[114:115], v[66:67]
	v_pk_fma_f32 v[28:29], v[48:49], v[64:65], v[68:69]
	global_store_dwordx4 v[104:105], v[0:3], off
	global_store_dwordx4 v[104:105], v[4:7], off offset:1024
	global_store_dwordx4 v[104:105], v[8:11], off offset:2048
	global_store_dwordx4 v[104:105], v[12:15], off offset:3072
	global_store_dwordx4 v[98:99], v[16:19], off
	global_store_dwordx4 v[98:99], v[20:23], off offset:1024
	global_store_dwordx4 v[98:99], v[24:27], off offset:2048
	global_store_dwordx4 v[98:99], v[28:31], off offset:3072
	s_cbranch_scc1 .LBB0_1557
